# baseline (speedup 1.0000x reference)
_Z8gat_mainPKiPKDF16_PKfS4_Pf:
	s_load_dwordx8 s[24:31], s[0:1], 0x0
	s_load_dwordx2 s[12:13], s[0:1], 0x20
	v_and_b32_e32 v2, 63, v0
	v_readfirstlane_b32 s16, v0
	v_lshlrev_b32_e32 v1, 4, v2
	s_lshr_b32 s16, s16, 6
	s_and_b32 s17, s2, 7
	s_lshr_b32 s18, s2, 3
	s_lshr_b32 s19, s18, 3
	s_add_u32 s19, s19, s18
	s_and_b32 s19, s19, 7
	s_lshr_b32 s20, s16, 2
	s_and_b32 s21, s16, 3
	s_lshl_b32 s22, s16, 16
	s_lshl_b32 s23, s16, 12
	s_lshl_b32 s58, s17, 24
	s_lshl_b32 s57, s18, 19
	s_add_u32 s58, s58, s57
	s_lshl_b32 s59, s17, 18
	s_lshl_b32 s72, s17, 11
	s_lshl_b32 s57, s18, 6
	s_add_u32 s72, s72, s57
	s_lshl_b32 s57, s16, 3
	s_add_u32 s72, s72, s57
	s_lshl_b32 s72, s72, 2
	s_lshl_b32 s73, s17, 13
	v_and_b32_e32 v36, 7, v0
	v_lshlrev_b32_e32 v36, 2, v36
	v_lshlrev_b32_e32 v38, 4, v0
	s_mov_b32 s6, 0x80000
	s_mov_b32 s7, 0x20000
	s_mov_b32 s10, 0x40000
	s_mov_b32 s11, 0x20000
	s_add_u32 s3, s19, 0
	s_and_b32 s3, s3, 7
	s_lshl_b32 s57, s3, 10
	s_add_u32 s48, s57, s22
	s_add_u32 s49, s48, 0x2000
	s_add_u32 s50, s48, 0x4000
	s_add_u32 s51, s48, 0x6000
	s_add_u32 s52, s48, 0x8000
	s_add_u32 s53, s48, 0xa000
	s_add_u32 s54, s48, 0xc000
	s_add_u32 s55, s48, 0xe000
	s_lshl_b32 s56, s3, 15
	s_add_u32 s56, s56, s23
	s_waitcnt lgkmcnt(0)
	s_add_u32 s28, s28, s72
	s_addc_u32 s29, s29, 0
	global_load_dword v37, v36, s[28:29]
	s_add_u32 s30, s30, s73
	s_addc_u32 s31, s31, 0
	global_load_dwordx4 v[24:27], v38, s[30:31]
	s_add_u32 s4, s24, s58
	s_addc_u32 s5, s25, 0
	s_and_b32 s5, s5, 0xffff
	buffer_load_dwordx4 v[88:91], v1, s[4:7], s48 offen nt
	buffer_load_dwordx4 v[92:95], v1, s[4:7], s49 offen nt
	buffer_load_dwordx4 v[96:99], v1, s[4:7], s50 offen nt
	buffer_load_dwordx4 v[100:103], v1, s[4:7], s51 offen nt
	buffer_load_dwordx4 v[104:107], v1, s[4:7], s52 offen nt
	buffer_load_dwordx4 v[108:111], v1, s[4:7], s53 offen nt
	buffer_load_dwordx4 v[112:115], v1, s[4:7], s54 offen nt
	buffer_load_dwordx4 v[116:119], v1, s[4:7], s55 offen nt
	s_add_u32 s8, s26, s59
	s_addc_u32 s9, s27, 0
	s_and_b32 s9, s9, 0xffff
	buffer_load_dwordx4 v[152:155], v1, s[8:11], s56 offen
	buffer_load_dwordx4 v[156:159], v1, s[8:11], s56 offen offset:1024
	buffer_load_dwordx4 v[160:163], v1, s[8:11], s56 offen offset:2048
	buffer_load_dwordx4 v[164:167], v1, s[8:11], s56 offen offset:3072
	s_mul_i32 s3, s16, 0x1080
	v_lshlrev_b32_e32 v3, 3, v2
	v_add_u32_e32 v3, s3, v3
	v_add_u32_e32 v4, 0x840, v3
	v_add_u32_e32 v5, 0x8400, v3
	v_add_u32_e32 v6, 0x8400, v4
	v_and_b32_e32 v36, 31, v2
	v_mul_u32_u24_e32 v36, 0x210, v36
	v_lshrrev_b32_e32 v38, 5, v2
	v_lshlrev_b32_e32 v38, 4, v38
	v_add_u32_e32 v7, v36, v38
	s_mul_i32 s3, s20, 0x4200
	s_lshl_b32 s57, s21, 7
	s_add_u32 s3, s3, s57
	v_add_u32_e32 v7, s3, v7
	s_lshl_b32 s3, s21, 13
	s_add_u32 s3, s3, 0x14800
	v_add_u32_e32 v8, s3, v1
	s_add_u32 s3, s23, 0x14800
	v_add_u32_e32 v9, s3, v1
	v_add_u32_e32 v10, 0x10800, v1
	v_mov_b32_e32 v12, 0x3c003c00
	v_mov_b32_e32 v13, 0x3c003c00
	v_mov_b32_e32 v14, 0x3c003c00
	v_mov_b32_e32 v15, 0x3c003c00
	v_mov_b32_e32 v40, 0
	v_mov_b32_e32 v41, 0
	v_mov_b32_e32 v42, 0
	v_mov_b32_e32 v43, 0
	v_mov_b32_e32 v44, 0
	v_mov_b32_e32 v45, 0
	v_mov_b32_e32 v46, 0
	v_mov_b32_e32 v47, 0
	v_mov_b32_e32 v48, 0
	v_mov_b32_e32 v49, 0
	v_mov_b32_e32 v50, 0
	v_mov_b32_e32 v51, 0
	v_mov_b32_e32 v52, 0
	v_mov_b32_e32 v53, 0
	v_mov_b32_e32 v54, 0
	v_mov_b32_e32 v55, 0
	v_mov_b32_e32 v56, 0
	v_mov_b32_e32 v57, 0
	v_mov_b32_e32 v58, 0
	v_mov_b32_e32 v59, 0
	v_mov_b32_e32 v60, 0
	v_mov_b32_e32 v61, 0
	v_mov_b32_e32 v62, 0
	v_mov_b32_e32 v63, 0
	v_mov_b32_e32 v64, 0
	v_mov_b32_e32 v65, 0
	v_mov_b32_e32 v66, 0
	v_mov_b32_e32 v67, 0
	v_mov_b32_e32 v68, 0
	v_mov_b32_e32 v69, 0
	v_mov_b32_e32 v70, 0
	v_mov_b32_e32 v71, 0
	v_mov_b32_e32 v72, 0
	v_mov_b32_e32 v73, 0
	v_mov_b32_e32 v74, 0
	v_mov_b32_e32 v75, 0
	v_mov_b32_e32 v76, 0
	v_mov_b32_e32 v77, 0
	v_mov_b32_e32 v78, 0
	v_mov_b32_e32 v79, 0
	v_mov_b32_e32 v80, 0
	v_mov_b32_e32 v81, 0
	v_mov_b32_e32 v82, 0
	v_mov_b32_e32 v83, 0
	v_mov_b32_e32 v84, 0
	v_mov_b32_e32 v85, 0
	v_mov_b32_e32 v86, 0
	v_mov_b32_e32 v87, 0
	s_lshl_b32 s3, s17, 11
	s_lshl_b32 s57, s18, 6
	s_add_u32 s3, s3, s57
	s_lshl_b32 s57, s20, 5
	s_add_u32 s3, s3, s57
	s_lshl_b32 s57, s21, 3
	s_add_u32 s3, s3, s57
	s_lshl_b32 s3, s3, 8
	s_add_u32 s12, s12, s3
	s_addc_u32 s13, s13, 0
	s_waitcnt vmcnt(12)
	v_max_f32_e32 v28, v24, v25
	v_max3_f32 v28, v28, v26, v27
	s_nop 1
	v_max_f32_dpp v29, v28, v28 quad_perm:[1,0,3,2] row_mask:0xf bank_mask:0xf
	s_nop 1
	v_max_f32_dpp v28, v29, v29 quad_perm:[2,3,0,1] row_mask:0xf bank_mask:0xf
	s_nop 1
	v_max_f32_dpp v29, v28, v28 row_half_mirror row_mask:0xf bank_mask:0xf
	s_nop 1
	v_max_f32_dpp v28, v29, v29 row_mirror row_mask:0xf bank_mask:0xf
	s_nop 1
	v_readlane_b32 s3, v28, 0
	v_readlane_b32 s57, v28, 16
	v_readlane_b32 s58, v28, 32
	v_readlane_b32 s59, v28, 48
	s_nop 1
	v_mov_b32_e32 v28, s3
	v_max_f32_e32 v28, s57, v28
	v_max_f32_e32 v28, s58, v28
	v_max_f32_e32 v28, s59, v28
	s_lshl_b32 s3, s16, 2
	s_add_u32 s3, s3, 0x24800
	v_mov_b32_e32 v30, s3
	ds_write_b32 v30, v28
	s_waitcnt lgkmcnt(0)
	s_barrier
	v_mov_b32_e32 v30, 0x24800
	ds_read_b128 v[32:35], v30
	ds_read_b128 v[16:19], v30 offset:16
	s_waitcnt lgkmcnt(0)
	v_max3_f32 v28, v32, v33, v34
	v_max3_f32 v28, v28, v35, v16
	v_max3_f32 v28, v28, v17, v18
	v_max_f32_e32 v28, v28, v19
	v_sub_f32_e32 v16, v24, v28
	v_sub_f32_e32 v17, v25, v28
	v_sub_f32_e32 v18, v26, v28
	v_sub_f32_e32 v19, v27, v28
	v_mul_f32_e32 v20, 0x3e4ccccd, v16
	v_mul_f32_e32 v21, 0x3e4ccccd, v17
	v_mul_f32_e32 v22, 0x3e4ccccd, v18
	v_mul_f32_e32 v23, 0x3e4ccccd, v19
	v_exp_f32_e32 v16, v16
	v_exp_f32_e32 v17, v17
	v_exp_f32_e32 v18, v18
	v_exp_f32_e32 v19, v19
	v_exp_f32_e32 v20, v20
	v_exp_f32_e32 v21, v21
	v_exp_f32_e32 v22, v22
	v_exp_f32_e32 v23, v23
	v_lshlrev_b32_e32 v30, 4, v0
	v_add_u32_e32 v30, 0x10800, v30
	ds_write_b128 v30, v[16:19]
	ds_write_b128 v30, v[20:23] offset:8192
	v_add_f32_e32 v36, v37, v28
	v_mul_f32_e32 v38, 0x3e4ccccd, v36
	v_max_f32_e32 v39, v36, v38
	v_sub_f32_e32 v36, v36, v39
	v_sub_f32_e32 v38, v38, v39
	v_add_f32_e32 v36, 0x41600000, v36
	v_add_f32_e32 v38, 0x41600000, v38
	v_exp_f32_e32 v36, v36
	v_exp_f32_e32 v38, v38
	s_nop 1
	v_readlane_b32 s32, v36, 0
	v_readlane_b32 s33, v36, 1
	v_readlane_b32 s34, v36, 2
	v_readlane_b32 s35, v36, 3
	v_readlane_b32 s36, v36, 4
	v_readlane_b32 s37, v36, 5
	v_readlane_b32 s38, v36, 6
	v_readlane_b32 s39, v36, 7
	v_readlane_b32 s40, v38, 0
	v_readlane_b32 s41, v38, 1
	v_readlane_b32 s42, v38, 2
	v_readlane_b32 s43, v38, 3
	v_readlane_b32 s44, v38, 4
	v_readlane_b32 s45, v38, 5
	v_readlane_b32 s46, v38, 6
	v_readlane_b32 s47, v38, 7
	s_waitcnt lgkmcnt(0)
	s_barrier
	s_lshl_b32 s3, s19, 10
	v_add_u32_e32 v11, s3, v10
	ds_read_b128 v[16:19], v11
	ds_read_b128 v[20:23], v11 offset:8192
	s_waitcnt lgkmcnt(0)
	s_add_u32 s3, s19, 1
	s_and_b32 s3, s3, 7
	s_lshl_b32 s57, s3, 10
	s_add_u32 s48, s57, s22
	s_add_u32 s49, s48, 0x2000
	s_add_u32 s50, s48, 0x4000
	s_add_u32 s51, s48, 0x6000
	s_add_u32 s52, s48, 0x8000
	s_add_u32 s53, s48, 0xa000
	s_add_u32 s54, s48, 0xc000
	s_add_u32 s55, s48, 0xe000
	s_lshl_b32 s56, s3, 15
	s_add_u32 s56, s56, s23
	buffer_load_dwordx4 v[120:123], v1, s[4:7], s48 offen nt
	buffer_load_dwordx4 v[124:127], v1, s[4:7], s49 offen nt
	buffer_load_dwordx4 v[128:131], v1, s[4:7], s50 offen nt
	buffer_load_dwordx4 v[132:135], v1, s[4:7], s51 offen nt
	buffer_load_dwordx4 v[136:139], v1, s[4:7], s52 offen nt
	buffer_load_dwordx4 v[140:143], v1, s[4:7], s53 offen nt
	buffer_load_dwordx4 v[144:147], v1, s[4:7], s54 offen nt
	buffer_load_dwordx4 v[148:151], v1, s[4:7], s55 offen nt
	buffer_load_dwordx4 v[168:171], v1, s[8:11], s56 offen
	buffer_load_dwordx4 v[172:175], v1, s[8:11], s56 offen offset:1024
	buffer_load_dwordx4 v[176:179], v1, s[8:11], s56 offen offset:2048
	buffer_load_dwordx4 v[180:183], v1, s[8:11], s56 offen offset:3072
	s_waitcnt vmcnt(16)
	v_pk_mul_f32 v[24:25], v[16:17], s[32:33] op_sel_hi:[1,0]
	v_pk_mul_f32 v[26:27], v[18:19], s[32:33] op_sel_hi:[1,0]
	v_pk_mul_f32 v[28:29], v[20:21], s[40:41] op_sel_hi:[1,0]
	v_pk_mul_f32 v[30:31], v[22:23], s[40:41] op_sel_hi:[1,0]
	v_cmp_lt_i32_e64 s[60:61], 0, v88
	v_cmp_lt_i32_e64 s[62:63], 0, v89
	v_cmp_lt_i32_e64 s[64:65], 0, v90
	v_cmp_lt_i32_e64 s[66:67], 0, v91
	v_max_f32_e32 v24, v24, v28
	v_max_f32_e32 v25, v25, v29
	v_max_f32_e32 v26, v26, v30
	v_max_f32_e32 v27, v27, v31
	v_cndmask_b32_e64 v24, 0, v24, s[60:61]
	v_cndmask_b32_e64 v25, 0, v25, s[62:63]
	v_cndmask_b32_e64 v26, 0, v26, s[64:65]
	v_cndmask_b32_e64 v27, 0, v27, s[66:67]
	v_cvt_pkrtz_f16_f32 v32, v24, v25
	v_cvt_pkrtz_f16_f32 v33, v26, v27
	v_pk_mul_f32 v[24:25], v[16:17], s[32:33] op_sel:[0,1] op_sel_hi:[1,1]
	v_pk_mul_f32 v[26:27], v[18:19], s[32:33] op_sel:[0,1] op_sel_hi:[1,1]
	v_pk_mul_f32 v[28:29], v[20:21], s[40:41] op_sel:[0,1] op_sel_hi:[1,1]
	v_pk_mul_f32 v[30:31], v[22:23], s[40:41] op_sel:[0,1] op_sel_hi:[1,1]
	v_cmp_lt_i32_e64 s[60:61], 0, v92
	v_cmp_lt_i32_e64 s[62:63], 0, v93
	v_cmp_lt_i32_e64 s[64:65], 0, v94
	v_cmp_lt_i32_e64 s[66:67], 0, v95
	v_max_f32_e32 v24, v24, v28
	v_max_f32_e32 v25, v25, v29
	v_max_f32_e32 v26, v26, v30
	v_max_f32_e32 v27, v27, v31
	v_cndmask_b32_e64 v24, 0, v24, s[60:61]
	v_cndmask_b32_e64 v25, 0, v25, s[62:63]
	v_cndmask_b32_e64 v26, 0, v26, s[64:65]
	v_cndmask_b32_e64 v27, 0, v27, s[66:67]
	v_cvt_pkrtz_f16_f32 v34, v24, v25
	v_cvt_pkrtz_f16_f32 v35, v26, v27
	ds_write2_b64 v3, v[32:33], v[34:35] offset0:0 offset1:66
	v_pk_mul_f32 v[24:25], v[16:17], s[34:35] op_sel_hi:[1,0]
	v_pk_mul_f32 v[26:27], v[18:19], s[34:35] op_sel_hi:[1,0]
	v_pk_mul_f32 v[28:29], v[20:21], s[42:43] op_sel_hi:[1,0]
	v_pk_mul_f32 v[30:31], v[22:23], s[42:43] op_sel_hi:[1,0]
	v_cmp_lt_i32_e64 s[60:61], 0, v96
	v_cmp_lt_i32_e64 s[62:63], 0, v97
	v_cmp_lt_i32_e64 s[64:65], 0, v98
	v_cmp_lt_i32_e64 s[66:67], 0, v99
	v_max_f32_e32 v24, v24, v28
	v_max_f32_e32 v25, v25, v29
	v_max_f32_e32 v26, v26, v30
	v_max_f32_e32 v27, v27, v31
	v_cndmask_b32_e64 v24, 0, v24, s[60:61]
	v_cndmask_b32_e64 v25, 0, v25, s[62:63]
	v_cndmask_b32_e64 v26, 0, v26, s[64:65]
	v_cndmask_b32_e64 v27, 0, v27, s[66:67]
	v_cvt_pkrtz_f16_f32 v32, v24, v25
	v_cvt_pkrtz_f16_f32 v33, v26, v27
	v_pk_mul_f32 v[24:25], v[16:17], s[34:35] op_sel:[0,1] op_sel_hi:[1,1]
	v_pk_mul_f32 v[26:27], v[18:19], s[34:35] op_sel:[0,1] op_sel_hi:[1,1]
	v_pk_mul_f32 v[28:29], v[20:21], s[42:43] op_sel:[0,1] op_sel_hi:[1,1]
	v_pk_mul_f32 v[30:31], v[22:23], s[42:43] op_sel:[0,1] op_sel_hi:[1,1]
	v_cmp_lt_i32_e64 s[60:61], 0, v100
	v_cmp_lt_i32_e64 s[62:63], 0, v101
	v_cmp_lt_i32_e64 s[64:65], 0, v102
	v_cmp_lt_i32_e64 s[66:67], 0, v103
	v_max_f32_e32 v24, v24, v28
	v_max_f32_e32 v25, v25, v29
	v_max_f32_e32 v26, v26, v30
	v_max_f32_e32 v27, v27, v31
	v_cndmask_b32_e64 v24, 0, v24, s[60:61]
	v_cndmask_b32_e64 v25, 0, v25, s[62:63]
	v_cndmask_b32_e64 v26, 0, v26, s[64:65]
	v_cndmask_b32_e64 v27, 0, v27, s[66:67]
	v_cvt_pkrtz_f16_f32 v34, v24, v25
	v_cvt_pkrtz_f16_f32 v35, v26, v27
	ds_write2_b64 v3, v[32:33], v[34:35] offset0:132 offset1:198
	v_pk_mul_f32 v[24:25], v[16:17], s[36:37] op_sel_hi:[1,0]
	v_pk_mul_f32 v[26:27], v[18:19], s[36:37] op_sel_hi:[1,0]
	v_pk_mul_f32 v[28:29], v[20:21], s[44:45] op_sel_hi:[1,0]
	v_pk_mul_f32 v[30:31], v[22:23], s[44:45] op_sel_hi:[1,0]
	v_cmp_lt_i32_e64 s[60:61], 0, v104
	v_cmp_lt_i32_e64 s[62:63], 0, v105
	v_cmp_lt_i32_e64 s[64:65], 0, v106
	v_cmp_lt_i32_e64 s[66:67], 0, v107
	v_max_f32_e32 v24, v24, v28
	v_max_f32_e32 v25, v25, v29
	v_max_f32_e32 v26, v26, v30
	v_max_f32_e32 v27, v27, v31
	v_cndmask_b32_e64 v24, 0, v24, s[60:61]
	v_cndmask_b32_e64 v25, 0, v25, s[62:63]
	v_cndmask_b32_e64 v26, 0, v26, s[64:65]
	v_cndmask_b32_e64 v27, 0, v27, s[66:67]
	v_cvt_pkrtz_f16_f32 v32, v24, v25
	v_cvt_pkrtz_f16_f32 v33, v26, v27
	v_pk_mul_f32 v[24:25], v[16:17], s[36:37] op_sel:[0,1] op_sel_hi:[1,1]
	v_pk_mul_f32 v[26:27], v[18:19], s[36:37] op_sel:[0,1] op_sel_hi:[1,1]
	v_pk_mul_f32 v[28:29], v[20:21], s[44:45] op_sel:[0,1] op_sel_hi:[1,1]
	v_pk_mul_f32 v[30:31], v[22:23], s[44:45] op_sel:[0,1] op_sel_hi:[1,1]
	v_cmp_lt_i32_e64 s[60:61], 0, v108
	v_cmp_lt_i32_e64 s[62:63], 0, v109
	v_cmp_lt_i32_e64 s[64:65], 0, v110
	v_cmp_lt_i32_e64 s[66:67], 0, v111
	v_max_f32_e32 v24, v24, v28
	v_max_f32_e32 v25, v25, v29
	v_max_f32_e32 v26, v26, v30
	v_max_f32_e32 v27, v27, v31
	v_cndmask_b32_e64 v24, 0, v24, s[60:61]
	v_cndmask_b32_e64 v25, 0, v25, s[62:63]
	v_cndmask_b32_e64 v26, 0, v26, s[64:65]
	v_cndmask_b32_e64 v27, 0, v27, s[66:67]
	v_cvt_pkrtz_f16_f32 v34, v24, v25
	v_cvt_pkrtz_f16_f32 v35, v26, v27
	ds_write2_b64 v4, v[32:33], v[34:35] offset0:0 offset1:66
	v_pk_mul_f32 v[24:25], v[16:17], s[38:39] op_sel_hi:[1,0]
	v_pk_mul_f32 v[26:27], v[18:19], s[38:39] op_sel_hi:[1,0]
	v_pk_mul_f32 v[28:29], v[20:21], s[46:47] op_sel_hi:[1,0]
	v_pk_mul_f32 v[30:31], v[22:23], s[46:47] op_sel_hi:[1,0]
	v_cmp_lt_i32_e64 s[60:61], 0, v112
	v_cmp_lt_i32_e64 s[62:63], 0, v113
	v_cmp_lt_i32_e64 s[64:65], 0, v114
	v_cmp_lt_i32_e64 s[66:67], 0, v115
	v_max_f32_e32 v24, v24, v28
	v_max_f32_e32 v25, v25, v29
	v_max_f32_e32 v26, v26, v30
	v_max_f32_e32 v27, v27, v31
	v_cndmask_b32_e64 v24, 0, v24, s[60:61]
	v_cndmask_b32_e64 v25, 0, v25, s[62:63]
	v_cndmask_b32_e64 v26, 0, v26, s[64:65]
	v_cndmask_b32_e64 v27, 0, v27, s[66:67]
	v_cvt_pkrtz_f16_f32 v32, v24, v25
	v_cvt_pkrtz_f16_f32 v33, v26, v27
	v_pk_mul_f32 v[24:25], v[16:17], s[38:39] op_sel:[0,1] op_sel_hi:[1,1]
	v_pk_mul_f32 v[26:27], v[18:19], s[38:39] op_sel:[0,1] op_sel_hi:[1,1]
	v_pk_mul_f32 v[28:29], v[20:21], s[46:47] op_sel:[0,1] op_sel_hi:[1,1]
	v_pk_mul_f32 v[30:31], v[22:23], s[46:47] op_sel:[0,1] op_sel_hi:[1,1]
	v_cmp_lt_i32_e64 s[60:61], 0, v116
	v_cmp_lt_i32_e64 s[62:63], 0, v117
	v_cmp_lt_i32_e64 s[64:65], 0, v118
	v_cmp_lt_i32_e64 s[66:67], 0, v119
	v_max_f32_e32 v24, v24, v28
	v_max_f32_e32 v25, v25, v29
	v_max_f32_e32 v26, v26, v30
	v_max_f32_e32 v27, v27, v31
	v_cndmask_b32_e64 v24, 0, v24, s[60:61]
	v_cndmask_b32_e64 v25, 0, v25, s[62:63]
	v_cndmask_b32_e64 v26, 0, v26, s[64:65]
	v_cndmask_b32_e64 v27, 0, v27, s[66:67]
	v_cvt_pkrtz_f16_f32 v34, v24, v25
	v_cvt_pkrtz_f16_f32 v35, v26, v27
	ds_write2_b64 v4, v[32:33], v[34:35] offset0:132 offset1:198
	s_waitcnt vmcnt(12)
	ds_write_b128 v9, v[152:155] offset:0
	ds_write_b128 v9, v[156:159] offset:1024
	ds_write_b128 v9, v[160:163] offset:2048
	ds_write_b128 v9, v[164:167] offset:3072
	s_add_u32 s3, s19, 1
	s_and_b32 s3, s3, 7
	s_lshl_b32 s3, s3, 10
	v_add_u32_e32 v11, s3, v10
	ds_read_b128 v[16:19], v11
	ds_read_b128 v[20:23], v11 offset:8192
	s_waitcnt lgkmcnt(0)
	s_barrier
	ds_read_b128 v[184:187], v7 offset:0
	ds_read_b128 v[200:203], v8 offset:0
	ds_read_b128 v[204:207], v8 offset:1024
	ds_read_b128 v[188:191], v7 offset:32
	ds_read_b128 v[208:211], v8 offset:2048
	ds_read_b128 v[212:215], v8 offset:3072
	ds_read_b128 v[192:195], v7 offset:64
	ds_read_b128 v[216:219], v8 offset:4096
	ds_read_b128 v[220:223], v8 offset:5120
	ds_read_b128 v[196:199], v7 offset:96
	ds_read_b128 v[224:227], v8 offset:6144
	ds_read_b128 v[228:231], v8 offset:7168
	s_add_u32 s3, s19, 2
	s_and_b32 s3, s3, 7
	s_lshl_b32 s57, s3, 10
	s_add_u32 s48, s57, s22
	s_add_u32 s49, s48, 0x2000
	s_add_u32 s50, s48, 0x4000
	s_add_u32 s51, s48, 0x6000
	s_add_u32 s52, s48, 0x8000
	s_add_u32 s53, s48, 0xa000
	s_add_u32 s54, s48, 0xc000
	s_add_u32 s55, s48, 0xe000
	s_lshl_b32 s56, s3, 15
	s_add_u32 s56, s56, s23
	buffer_load_dwordx4 v[88:91], v1, s[4:7], s48 offen nt
	buffer_load_dwordx4 v[92:95], v1, s[4:7], s49 offen nt
	buffer_load_dwordx4 v[96:99], v1, s[4:7], s50 offen nt
	buffer_load_dwordx4 v[100:103], v1, s[4:7], s51 offen nt
	buffer_load_dwordx4 v[104:107], v1, s[4:7], s52 offen nt
	buffer_load_dwordx4 v[108:111], v1, s[4:7], s53 offen nt
	buffer_load_dwordx4 v[112:115], v1, s[4:7], s54 offen nt
	buffer_load_dwordx4 v[116:119], v1, s[4:7], s55 offen nt
	buffer_load_dwordx4 v[152:155], v1, s[8:11], s56 offen
	buffer_load_dwordx4 v[156:159], v1, s[8:11], s56 offen offset:1024
	buffer_load_dwordx4 v[160:163], v1, s[8:11], s56 offen offset:2048
	buffer_load_dwordx4 v[164:167], v1, s[8:11], s56 offen offset:3072
	s_waitcnt vmcnt(12)
	v_pk_mul_f32 v[24:25], v[16:17], s[32:33] op_sel_hi:[1,0]
	v_pk_mul_f32 v[26:27], v[18:19], s[32:33] op_sel_hi:[1,0]
	v_pk_mul_f32 v[28:29], v[20:21], s[40:41] op_sel_hi:[1,0]
	v_pk_mul_f32 v[30:31], v[22:23], s[40:41] op_sel_hi:[1,0]
	v_cmp_lt_i32_e64 s[60:61], 0, v120
	v_cmp_lt_i32_e64 s[62:63], 0, v121
	v_cmp_lt_i32_e64 s[64:65], 0, v122
	v_cmp_lt_i32_e64 s[66:67], 0, v123
	v_max_f32_e32 v24, v24, v28
	v_max_f32_e32 v25, v25, v29
	v_max_f32_e32 v26, v26, v30
	v_max_f32_e32 v27, v27, v31
	v_cndmask_b32_e64 v24, 0, v24, s[60:61]
	v_cndmask_b32_e64 v25, 0, v25, s[62:63]
	v_cndmask_b32_e64 v26, 0, v26, s[64:65]
	v_cndmask_b32_e64 v27, 0, v27, s[66:67]
	v_cvt_pkrtz_f16_f32 v32, v24, v25
	v_cvt_pkrtz_f16_f32 v33, v26, v27
	s_waitcnt lgkmcnt(0)
	v_pk_mul_f32 v[24:25], v[16:17], s[32:33] op_sel:[0,1] op_sel_hi:[1,1]
	v_pk_mul_f32 v[26:27], v[18:19], s[32:33] op_sel:[0,1] op_sel_hi:[1,1]
	v_pk_mul_f32 v[28:29], v[20:21], s[40:41] op_sel:[0,1] op_sel_hi:[1,1]
	v_pk_mul_f32 v[30:31], v[22:23], s[40:41] op_sel:[0,1] op_sel_hi:[1,1]
	v_mfma_f32_32x32x16_f16 v[40:55], v[184:187], v[200:203], v[40:55]
	v_cmp_lt_i32_e64 s[60:61], 0, v124
	v_cmp_lt_i32_e64 s[62:63], 0, v125
	v_cmp_lt_i32_e64 s[64:65], 0, v126
	v_cmp_lt_i32_e64 s[66:67], 0, v127
	v_max_f32_e32 v24, v24, v28
	v_max_f32_e32 v25, v25, v29
	v_max_f32_e32 v26, v26, v30
	v_max_f32_e32 v27, v27, v31
	v_cndmask_b32_e64 v24, 0, v24, s[60:61]
	v_cndmask_b32_e64 v25, 0, v25, s[62:63]
	v_cndmask_b32_e64 v26, 0, v26, s[64:65]
	v_cndmask_b32_e64 v27, 0, v27, s[66:67]
	v_mfma_f32_32x32x16_f16 v[56:71], v[184:187], v[204:207], v[56:71]
	v_cvt_pkrtz_f16_f32 v34, v24, v25
	v_cvt_pkrtz_f16_f32 v35, v26, v27
	ds_write2_b64 v5, v[32:33], v[34:35] offset0:0 offset1:66
	v_pk_mul_f32 v[24:25], v[16:17], s[34:35] op_sel_hi:[1,0]
	v_pk_mul_f32 v[26:27], v[18:19], s[34:35] op_sel_hi:[1,0]
	v_pk_mul_f32 v[28:29], v[20:21], s[42:43] op_sel_hi:[1,0]
	v_pk_mul_f32 v[30:31], v[22:23], s[42:43] op_sel_hi:[1,0]
	v_mfma_f32_32x32x16_f16 v[72:87], v[184:187], v[12:15], v[72:87]
	v_cmp_lt_i32_e64 s[60:61], 0, v128
	v_cmp_lt_i32_e64 s[62:63], 0, v129
	v_cmp_lt_i32_e64 s[64:65], 0, v130
	v_cmp_lt_i32_e64 s[66:67], 0, v131
	v_max_f32_e32 v24, v24, v28
	v_max_f32_e32 v25, v25, v29
	v_max_f32_e32 v26, v26, v30
	v_max_f32_e32 v27, v27, v31
	v_cndmask_b32_e64 v24, 0, v24, s[60:61]
	v_cndmask_b32_e64 v25, 0, v25, s[62:63]
	v_cndmask_b32_e64 v26, 0, v26, s[64:65]
	v_cndmask_b32_e64 v27, 0, v27, s[66:67]
	v_mfma_f32_32x32x16_f16 v[40:55], v[188:191], v[208:211], v[40:55]
	v_cvt_pkrtz_f16_f32 v32, v24, v25
	v_cvt_pkrtz_f16_f32 v33, v26, v27
	v_pk_mul_f32 v[24:25], v[16:17], s[34:35] op_sel:[0,1] op_sel_hi:[1,1]
	v_pk_mul_f32 v[26:27], v[18:19], s[34:35] op_sel:[0,1] op_sel_hi:[1,1]
	v_pk_mul_f32 v[28:29], v[20:21], s[42:43] op_sel:[0,1] op_sel_hi:[1,1]
	v_pk_mul_f32 v[30:31], v[22:23], s[42:43] op_sel:[0,1] op_sel_hi:[1,1]
	v_mfma_f32_32x32x16_f16 v[56:71], v[188:191], v[212:215], v[56:71]
	v_cmp_lt_i32_e64 s[60:61], 0, v132
	v_cmp_lt_i32_e64 s[62:63], 0, v133
	v_cmp_lt_i32_e64 s[64:65], 0, v134
	v_cmp_lt_i32_e64 s[66:67], 0, v135
	v_max_f32_e32 v24, v24, v28
	v_max_f32_e32 v25, v25, v29
	v_max_f32_e32 v26, v26, v30
	v_max_f32_e32 v27, v27, v31
	v_cndmask_b32_e64 v24, 0, v24, s[60:61]
	v_cndmask_b32_e64 v25, 0, v25, s[62:63]
	v_cndmask_b32_e64 v26, 0, v26, s[64:65]
	v_cndmask_b32_e64 v27, 0, v27, s[66:67]
	v_mfma_f32_32x32x16_f16 v[72:87], v[188:191], v[12:15], v[72:87]
	v_cvt_pkrtz_f16_f32 v34, v24, v25
	v_cvt_pkrtz_f16_f32 v35, v26, v27
	ds_write2_b64 v5, v[32:33], v[34:35] offset0:132 offset1:198
	v_pk_mul_f32 v[24:25], v[16:17], s[36:37] op_sel_hi:[1,0]
	v_pk_mul_f32 v[26:27], v[18:19], s[36:37] op_sel_hi:[1,0]
	v_pk_mul_f32 v[28:29], v[20:21], s[44:45] op_sel_hi:[1,0]
	v_pk_mul_f32 v[30:31], v[22:23], s[44:45] op_sel_hi:[1,0]
	v_mfma_f32_32x32x16_f16 v[40:55], v[192:195], v[216:219], v[40:55]
	v_cmp_lt_i32_e64 s[60:61], 0, v136
	v_cmp_lt_i32_e64 s[62:63], 0, v137
	v_cmp_lt_i32_e64 s[64:65], 0, v138
	v_cmp_lt_i32_e64 s[66:67], 0, v139
	v_max_f32_e32 v24, v24, v28
	v_max_f32_e32 v25, v25, v29
	v_max_f32_e32 v26, v26, v30
	v_max_f32_e32 v27, v27, v31
	v_cndmask_b32_e64 v24, 0, v24, s[60:61]
	v_cndmask_b32_e64 v25, 0, v25, s[62:63]
	v_cndmask_b32_e64 v26, 0, v26, s[64:65]
	v_cndmask_b32_e64 v27, 0, v27, s[66:67]
	v_mfma_f32_32x32x16_f16 v[56:71], v[192:195], v[220:223], v[56:71]
	v_cvt_pkrtz_f16_f32 v32, v24, v25
	v_cvt_pkrtz_f16_f32 v33, v26, v27
	v_pk_mul_f32 v[24:25], v[16:17], s[36:37] op_sel:[0,1] op_sel_hi:[1,1]
	v_pk_mul_f32 v[26:27], v[18:19], s[36:37] op_sel:[0,1] op_sel_hi:[1,1]
	v_pk_mul_f32 v[28:29], v[20:21], s[44:45] op_sel:[0,1] op_sel_hi:[1,1]
	v_pk_mul_f32 v[30:31], v[22:23], s[44:45] op_sel:[0,1] op_sel_hi:[1,1]
	v_mfma_f32_32x32x16_f16 v[72:87], v[192:195], v[12:15], v[72:87]
	v_cmp_lt_i32_e64 s[60:61], 0, v140
	v_cmp_lt_i32_e64 s[62:63], 0, v141
	v_cmp_lt_i32_e64 s[64:65], 0, v142
	v_cmp_lt_i32_e64 s[66:67], 0, v143
	v_max_f32_e32 v24, v24, v28
	v_max_f32_e32 v25, v25, v29
	v_max_f32_e32 v26, v26, v30
	v_max_f32_e32 v27, v27, v31
	v_cndmask_b32_e64 v24, 0, v24, s[60:61]
	v_cndmask_b32_e64 v25, 0, v25, s[62:63]
	v_cndmask_b32_e64 v26, 0, v26, s[64:65]
	v_cndmask_b32_e64 v27, 0, v27, s[66:67]
	v_mfma_f32_32x32x16_f16 v[40:55], v[196:199], v[224:227], v[40:55]
	v_cvt_pkrtz_f16_f32 v34, v24, v25
	v_cvt_pkrtz_f16_f32 v35, v26, v27
	ds_write2_b64 v6, v[32:33], v[34:35] offset0:0 offset1:66
	v_pk_mul_f32 v[24:25], v[16:17], s[38:39] op_sel_hi:[1,0]
	v_pk_mul_f32 v[26:27], v[18:19], s[38:39] op_sel_hi:[1,0]
	v_pk_mul_f32 v[28:29], v[20:21], s[46:47] op_sel_hi:[1,0]
	v_pk_mul_f32 v[30:31], v[22:23], s[46:47] op_sel_hi:[1,0]
	v_mfma_f32_32x32x16_f16 v[56:71], v[196:199], v[228:231], v[56:71]
	v_cmp_lt_i32_e64 s[60:61], 0, v144
	v_cmp_lt_i32_e64 s[62:63], 0, v145
	v_cmp_lt_i32_e64 s[64:65], 0, v146
	v_cmp_lt_i32_e64 s[66:67], 0, v147
	v_max_f32_e32 v24, v24, v28
	v_max_f32_e32 v25, v25, v29
	v_max_f32_e32 v26, v26, v30
	v_max_f32_e32 v27, v27, v31
	v_cndmask_b32_e64 v24, 0, v24, s[60:61]
	v_cndmask_b32_e64 v25, 0, v25, s[62:63]
	v_cndmask_b32_e64 v26, 0, v26, s[64:65]
	v_cndmask_b32_e64 v27, 0, v27, s[66:67]
	v_cvt_pkrtz_f16_f32 v32, v24, v25
	v_cvt_pkrtz_f16_f32 v33, v26, v27
	v_pk_mul_f32 v[24:25], v[16:17], s[38:39] op_sel:[0,1] op_sel_hi:[1,1]
	v_pk_mul_f32 v[26:27], v[18:19], s[38:39] op_sel:[0,1] op_sel_hi:[1,1]
	v_pk_mul_f32 v[28:29], v[20:21], s[46:47] op_sel:[0,1] op_sel_hi:[1,1]
	v_pk_mul_f32 v[30:31], v[22:23], s[46:47] op_sel:[0,1] op_sel_hi:[1,1]
	v_mfma_f32_32x32x16_f16 v[72:87], v[196:199], v[12:15], v[72:87]
	v_cmp_lt_i32_e64 s[60:61], 0, v148
	v_cmp_lt_i32_e64 s[62:63], 0, v149
	v_cmp_lt_i32_e64 s[64:65], 0, v150
	v_cmp_lt_i32_e64 s[66:67], 0, v151
	v_max_f32_e32 v24, v24, v28
	v_max_f32_e32 v25, v25, v29
	v_max_f32_e32 v26, v26, v30
	v_max_f32_e32 v27, v27, v31
	v_cndmask_b32_e64 v24, 0, v24, s[60:61]
	v_cndmask_b32_e64 v25, 0, v25, s[62:63]
	v_cndmask_b32_e64 v26, 0, v26, s[64:65]
	v_cndmask_b32_e64 v27, 0, v27, s[66:67]
	v_cvt_pkrtz_f16_f32 v34, v24, v25
	v_cvt_pkrtz_f16_f32 v35, v26, v27
	ds_write2_b64 v6, v[32:33], v[34:35] offset0:132 offset1:198
	ds_write_b128 v9, v[168:171] offset:32768
	ds_write_b128 v9, v[172:175] offset:33792
	ds_write_b128 v9, v[176:179] offset:34816
	ds_write_b128 v9, v[180:183] offset:35840
	s_add_u32 s3, s19, 2
	s_and_b32 s3, s3, 7
	s_lshl_b32 s3, s3, 10
	v_add_u32_e32 v11, s3, v10
	ds_read_b128 v[16:19], v11
	ds_read_b128 v[20:23], v11 offset:8192
	s_waitcnt lgkmcnt(0)
	s_barrier
	ds_read_b128 v[184:187], v7 offset:33792
	ds_read_b128 v[200:203], v8 offset:32768
	ds_read_b128 v[204:207], v8 offset:33792
	ds_read_b128 v[188:191], v7 offset:33824
	ds_read_b128 v[208:211], v8 offset:34816
	ds_read_b128 v[212:215], v8 offset:35840
	ds_read_b128 v[192:195], v7 offset:33856
	ds_read_b128 v[216:219], v8 offset:36864
	ds_read_b128 v[220:223], v8 offset:37888
	ds_read_b128 v[196:199], v7 offset:33888
	ds_read_b128 v[224:227], v8 offset:38912
	ds_read_b128 v[228:231], v8 offset:39936
	s_add_u32 s3, s19, 3
	s_and_b32 s3, s3, 7
	s_lshl_b32 s57, s3, 10
	s_add_u32 s48, s57, s22
	s_add_u32 s49, s48, 0x2000
	s_add_u32 s50, s48, 0x4000
	s_add_u32 s51, s48, 0x6000
	s_add_u32 s52, s48, 0x8000
	s_add_u32 s53, s48, 0xa000
	s_add_u32 s54, s48, 0xc000
	s_add_u32 s55, s48, 0xe000
	s_lshl_b32 s56, s3, 15
	s_add_u32 s56, s56, s23
	buffer_load_dwordx4 v[120:123], v1, s[4:7], s48 offen nt
	buffer_load_dwordx4 v[124:127], v1, s[4:7], s49 offen nt
	buffer_load_dwordx4 v[128:131], v1, s[4:7], s50 offen nt
	buffer_load_dwordx4 v[132:135], v1, s[4:7], s51 offen nt
	buffer_load_dwordx4 v[136:139], v1, s[4:7], s52 offen nt
	buffer_load_dwordx4 v[140:143], v1, s[4:7], s53 offen nt
	buffer_load_dwordx4 v[144:147], v1, s[4:7], s54 offen nt
	buffer_load_dwordx4 v[148:151], v1, s[4:7], s55 offen nt
	buffer_load_dwordx4 v[168:171], v1, s[8:11], s56 offen
	buffer_load_dwordx4 v[172:175], v1, s[8:11], s56 offen offset:1024
	buffer_load_dwordx4 v[176:179], v1, s[8:11], s56 offen offset:2048
	buffer_load_dwordx4 v[180:183], v1, s[8:11], s56 offen offset:3072
	s_waitcnt vmcnt(12)
	v_pk_mul_f32 v[24:25], v[16:17], s[32:33] op_sel_hi:[1,0]
	v_pk_mul_f32 v[26:27], v[18:19], s[32:33] op_sel_hi:[1,0]
	v_pk_mul_f32 v[28:29], v[20:21], s[40:41] op_sel_hi:[1,0]
	v_pk_mul_f32 v[30:31], v[22:23], s[40:41] op_sel_hi:[1,0]
	v_cmp_lt_i32_e64 s[60:61], 0, v88
	v_cmp_lt_i32_e64 s[62:63], 0, v89
	v_cmp_lt_i32_e64 s[64:65], 0, v90
	v_cmp_lt_i32_e64 s[66:67], 0, v91
	v_max_f32_e32 v24, v24, v28
	v_max_f32_e32 v25, v25, v29
	v_max_f32_e32 v26, v26, v30
	v_max_f32_e32 v27, v27, v31
	v_cndmask_b32_e64 v24, 0, v24, s[60:61]
	v_cndmask_b32_e64 v25, 0, v25, s[62:63]
	v_cndmask_b32_e64 v26, 0, v26, s[64:65]
	v_cndmask_b32_e64 v27, 0, v27, s[66:67]
	v_cvt_pkrtz_f16_f32 v32, v24, v25
	v_cvt_pkrtz_f16_f32 v33, v26, v27
	s_waitcnt lgkmcnt(0)
	v_pk_mul_f32 v[24:25], v[16:17], s[32:33] op_sel:[0,1] op_sel_hi:[1,1]
	v_pk_mul_f32 v[26:27], v[18:19], s[32:33] op_sel:[0,1] op_sel_hi:[1,1]
	v_pk_mul_f32 v[28:29], v[20:21], s[40:41] op_sel:[0,1] op_sel_hi:[1,1]
	v_pk_mul_f32 v[30:31], v[22:23], s[40:41] op_sel:[0,1] op_sel_hi:[1,1]
	v_mfma_f32_32x32x16_f16 v[40:55], v[184:187], v[200:203], v[40:55]
	v_cmp_lt_i32_e64 s[60:61], 0, v92
	v_cmp_lt_i32_e64 s[62:63], 0, v93
	v_cmp_lt_i32_e64 s[64:65], 0, v94
	v_cmp_lt_i32_e64 s[66:67], 0, v95
	v_max_f32_e32 v24, v24, v28
	v_max_f32_e32 v25, v25, v29
	v_max_f32_e32 v26, v26, v30
	v_max_f32_e32 v27, v27, v31
	v_cndmask_b32_e64 v24, 0, v24, s[60:61]
	v_cndmask_b32_e64 v25, 0, v25, s[62:63]
	v_cndmask_b32_e64 v26, 0, v26, s[64:65]
	v_cndmask_b32_e64 v27, 0, v27, s[66:67]
	v_mfma_f32_32x32x16_f16 v[56:71], v[184:187], v[204:207], v[56:71]
	v_cvt_pkrtz_f16_f32 v34, v24, v25
	v_cvt_pkrtz_f16_f32 v35, v26, v27
	ds_write2_b64 v3, v[32:33], v[34:35] offset0:0 offset1:66
	v_pk_mul_f32 v[24:25], v[16:17], s[34:35] op_sel_hi:[1,0]
	v_pk_mul_f32 v[26:27], v[18:19], s[34:35] op_sel_hi:[1,0]
	v_pk_mul_f32 v[28:29], v[20:21], s[42:43] op_sel_hi:[1,0]
	v_pk_mul_f32 v[30:31], v[22:23], s[42:43] op_sel_hi:[1,0]
	v_mfma_f32_32x32x16_f16 v[72:87], v[184:187], v[12:15], v[72:87]
	v_cmp_lt_i32_e64 s[60:61], 0, v96
	v_cmp_lt_i32_e64 s[62:63], 0, v97
	v_cmp_lt_i32_e64 s[64:65], 0, v98
	v_cmp_lt_i32_e64 s[66:67], 0, v99
	v_max_f32_e32 v24, v24, v28
	v_max_f32_e32 v25, v25, v29
	v_max_f32_e32 v26, v26, v30
	v_max_f32_e32 v27, v27, v31
	v_cndmask_b32_e64 v24, 0, v24, s[60:61]
	v_cndmask_b32_e64 v25, 0, v25, s[62:63]
	v_cndmask_b32_e64 v26, 0, v26, s[64:65]
	v_cndmask_b32_e64 v27, 0, v27, s[66:67]
	v_mfma_f32_32x32x16_f16 v[40:55], v[188:191], v[208:211], v[40:55]
	v_cvt_pkrtz_f16_f32 v32, v24, v25
	v_cvt_pkrtz_f16_f32 v33, v26, v27
	v_pk_mul_f32 v[24:25], v[16:17], s[34:35] op_sel:[0,1] op_sel_hi:[1,1]
	v_pk_mul_f32 v[26:27], v[18:19], s[34:35] op_sel:[0,1] op_sel_hi:[1,1]
	v_pk_mul_f32 v[28:29], v[20:21], s[42:43] op_sel:[0,1] op_sel_hi:[1,1]
	v_pk_mul_f32 v[30:31], v[22:23], s[42:43] op_sel:[0,1] op_sel_hi:[1,1]
	v_mfma_f32_32x32x16_f16 v[56:71], v[188:191], v[212:215], v[56:71]
	v_cmp_lt_i32_e64 s[60:61], 0, v100
	v_cmp_lt_i32_e64 s[62:63], 0, v101
	v_cmp_lt_i32_e64 s[64:65], 0, v102
	v_cmp_lt_i32_e64 s[66:67], 0, v103
	v_max_f32_e32 v24, v24, v28
	v_max_f32_e32 v25, v25, v29
	v_max_f32_e32 v26, v26, v30
	v_max_f32_e32 v27, v27, v31
	v_cndmask_b32_e64 v24, 0, v24, s[60:61]
	v_cndmask_b32_e64 v25, 0, v25, s[62:63]
	v_cndmask_b32_e64 v26, 0, v26, s[64:65]
	v_cndmask_b32_e64 v27, 0, v27, s[66:67]
	v_mfma_f32_32x32x16_f16 v[72:87], v[188:191], v[12:15], v[72:87]
	v_cvt_pkrtz_f16_f32 v34, v24, v25
	v_cvt_pkrtz_f16_f32 v35, v26, v27
	ds_write2_b64 v3, v[32:33], v[34:35] offset0:132 offset1:198
	v_pk_mul_f32 v[24:25], v[16:17], s[36:37] op_sel_hi:[1,0]
	v_pk_mul_f32 v[26:27], v[18:19], s[36:37] op_sel_hi:[1,0]
	v_pk_mul_f32 v[28:29], v[20:21], s[44:45] op_sel_hi:[1,0]
	v_pk_mul_f32 v[30:31], v[22:23], s[44:45] op_sel_hi:[1,0]
	v_mfma_f32_32x32x16_f16 v[40:55], v[192:195], v[216:219], v[40:55]
	v_cmp_lt_i32_e64 s[60:61], 0, v104
	v_cmp_lt_i32_e64 s[62:63], 0, v105
	v_cmp_lt_i32_e64 s[64:65], 0, v106
	v_cmp_lt_i32_e64 s[66:67], 0, v107
	v_max_f32_e32 v24, v24, v28
	v_max_f32_e32 v25, v25, v29
	v_max_f32_e32 v26, v26, v30
	v_max_f32_e32 v27, v27, v31
	v_cndmask_b32_e64 v24, 0, v24, s[60:61]
	v_cndmask_b32_e64 v25, 0, v25, s[62:63]
	v_cndmask_b32_e64 v26, 0, v26, s[64:65]
	v_cndmask_b32_e64 v27, 0, v27, s[66:67]
	v_mfma_f32_32x32x16_f16 v[56:71], v[192:195], v[220:223], v[56:71]
	v_cvt_pkrtz_f16_f32 v32, v24, v25
	v_cvt_pkrtz_f16_f32 v33, v26, v27
	v_pk_mul_f32 v[24:25], v[16:17], s[36:37] op_sel:[0,1] op_sel_hi:[1,1]
	v_pk_mul_f32 v[26:27], v[18:19], s[36:37] op_sel:[0,1] op_sel_hi:[1,1]
	v_pk_mul_f32 v[28:29], v[20:21], s[44:45] op_sel:[0,1] op_sel_hi:[1,1]
	v_pk_mul_f32 v[30:31], v[22:23], s[44:45] op_sel:[0,1] op_sel_hi:[1,1]
	v_mfma_f32_32x32x16_f16 v[72:87], v[192:195], v[12:15], v[72:87]
	v_cmp_lt_i32_e64 s[60:61], 0, v108
	v_cmp_lt_i32_e64 s[62:63], 0, v109
	v_cmp_lt_i32_e64 s[64:65], 0, v110
	v_cmp_lt_i32_e64 s[66:67], 0, v111
	v_max_f32_e32 v24, v24, v28
	v_max_f32_e32 v25, v25, v29
	v_max_f32_e32 v26, v26, v30
	v_max_f32_e32 v27, v27, v31
	v_cndmask_b32_e64 v24, 0, v24, s[60:61]
	v_cndmask_b32_e64 v25, 0, v25, s[62:63]
	v_cndmask_b32_e64 v26, 0, v26, s[64:65]
	v_cndmask_b32_e64 v27, 0, v27, s[66:67]
	v_mfma_f32_32x32x16_f16 v[40:55], v[196:199], v[224:227], v[40:55]
	v_cvt_pkrtz_f16_f32 v34, v24, v25
	v_cvt_pkrtz_f16_f32 v35, v26, v27
	ds_write2_b64 v4, v[32:33], v[34:35] offset0:0 offset1:66
	v_pk_mul_f32 v[24:25], v[16:17], s[38:39] op_sel_hi:[1,0]
	v_pk_mul_f32 v[26:27], v[18:19], s[38:39] op_sel_hi:[1,0]
	v_pk_mul_f32 v[28:29], v[20:21], s[46:47] op_sel_hi:[1,0]
	v_pk_mul_f32 v[30:31], v[22:23], s[46:47] op_sel_hi:[1,0]
	v_mfma_f32_32x32x16_f16 v[56:71], v[196:199], v[228:231], v[56:71]
	v_cmp_lt_i32_e64 s[60:61], 0, v112
	v_cmp_lt_i32_e64 s[62:63], 0, v113
	v_cmp_lt_i32_e64 s[64:65], 0, v114
	v_cmp_lt_i32_e64 s[66:67], 0, v115
	v_max_f32_e32 v24, v24, v28
	v_max_f32_e32 v25, v25, v29
	v_max_f32_e32 v26, v26, v30
	v_max_f32_e32 v27, v27, v31
	v_cndmask_b32_e64 v24, 0, v24, s[60:61]
	v_cndmask_b32_e64 v25, 0, v25, s[62:63]
	v_cndmask_b32_e64 v26, 0, v26, s[64:65]
	v_cndmask_b32_e64 v27, 0, v27, s[66:67]
	v_cvt_pkrtz_f16_f32 v32, v24, v25
	v_cvt_pkrtz_f16_f32 v33, v26, v27
	v_pk_mul_f32 v[24:25], v[16:17], s[38:39] op_sel:[0,1] op_sel_hi:[1,1]
	v_pk_mul_f32 v[26:27], v[18:19], s[38:39] op_sel:[0,1] op_sel_hi:[1,1]
	v_pk_mul_f32 v[28:29], v[20:21], s[46:47] op_sel:[0,1] op_sel_hi:[1,1]
	v_pk_mul_f32 v[30:31], v[22:23], s[46:47] op_sel:[0,1] op_sel_hi:[1,1]
	v_mfma_f32_32x32x16_f16 v[72:87], v[196:199], v[12:15], v[72:87]
	v_cmp_lt_i32_e64 s[60:61], 0, v116
	v_cmp_lt_i32_e64 s[62:63], 0, v117
	v_cmp_lt_i32_e64 s[64:65], 0, v118
	v_cmp_lt_i32_e64 s[66:67], 0, v119
	v_max_f32_e32 v24, v24, v28
	v_max_f32_e32 v25, v25, v29
	v_max_f32_e32 v26, v26, v30
	v_max_f32_e32 v27, v27, v31
	v_cndmask_b32_e64 v24, 0, v24, s[60:61]
	v_cndmask_b32_e64 v25, 0, v25, s[62:63]
	v_cndmask_b32_e64 v26, 0, v26, s[64:65]
	v_cndmask_b32_e64 v27, 0, v27, s[66:67]
	v_cvt_pkrtz_f16_f32 v34, v24, v25
	v_cvt_pkrtz_f16_f32 v35, v26, v27
	ds_write2_b64 v4, v[32:33], v[34:35] offset0:132 offset1:198
	ds_write_b128 v9, v[152:155] offset:0
	ds_write_b128 v9, v[156:159] offset:1024
	ds_write_b128 v9, v[160:163] offset:2048
	ds_write_b128 v9, v[164:167] offset:3072
	s_add_u32 s3, s19, 3
	s_and_b32 s3, s3, 7
	s_lshl_b32 s3, s3, 10
	v_add_u32_e32 v11, s3, v10
	ds_read_b128 v[16:19], v11
	ds_read_b128 v[20:23], v11 offset:8192
	s_waitcnt lgkmcnt(0)
	s_barrier
	ds_read_b128 v[184:187], v7 offset:0
	ds_read_b128 v[200:203], v8 offset:0
	ds_read_b128 v[204:207], v8 offset:1024
	ds_read_b128 v[188:191], v7 offset:32
	ds_read_b128 v[208:211], v8 offset:2048
	ds_read_b128 v[212:215], v8 offset:3072
	ds_read_b128 v[192:195], v7 offset:64
	ds_read_b128 v[216:219], v8 offset:4096
	ds_read_b128 v[220:223], v8 offset:5120
	ds_read_b128 v[196:199], v7 offset:96
	ds_read_b128 v[224:227], v8 offset:6144
	ds_read_b128 v[228:231], v8 offset:7168
	s_add_u32 s3, s19, 4
	s_and_b32 s3, s3, 7
	s_lshl_b32 s57, s3, 10
	s_add_u32 s48, s57, s22
	s_add_u32 s49, s48, 0x2000
	s_add_u32 s50, s48, 0x4000
	s_add_u32 s51, s48, 0x6000
	s_add_u32 s52, s48, 0x8000
	s_add_u32 s53, s48, 0xa000
	s_add_u32 s54, s48, 0xc000
	s_add_u32 s55, s48, 0xe000
	s_lshl_b32 s56, s3, 15
	s_add_u32 s56, s56, s23
	buffer_load_dwordx4 v[88:91], v1, s[4:7], s48 offen nt
	buffer_load_dwordx4 v[92:95], v1, s[4:7], s49 offen nt
	buffer_load_dwordx4 v[96:99], v1, s[4:7], s50 offen nt
	buffer_load_dwordx4 v[100:103], v1, s[4:7], s51 offen nt
	buffer_load_dwordx4 v[104:107], v1, s[4:7], s52 offen nt
	buffer_load_dwordx4 v[108:111], v1, s[4:7], s53 offen nt
	buffer_load_dwordx4 v[112:115], v1, s[4:7], s54 offen nt
	buffer_load_dwordx4 v[116:119], v1, s[4:7], s55 offen nt
	buffer_load_dwordx4 v[152:155], v1, s[8:11], s56 offen
	buffer_load_dwordx4 v[156:159], v1, s[8:11], s56 offen offset:1024
	buffer_load_dwordx4 v[160:163], v1, s[8:11], s56 offen offset:2048
	buffer_load_dwordx4 v[164:167], v1, s[8:11], s56 offen offset:3072
	s_waitcnt vmcnt(12)
	v_pk_mul_f32 v[24:25], v[16:17], s[32:33] op_sel_hi:[1,0]
	v_pk_mul_f32 v[26:27], v[18:19], s[32:33] op_sel_hi:[1,0]
	v_pk_mul_f32 v[28:29], v[20:21], s[40:41] op_sel_hi:[1,0]
	v_pk_mul_f32 v[30:31], v[22:23], s[40:41] op_sel_hi:[1,0]
	v_cmp_lt_i32_e64 s[60:61], 0, v120
	v_cmp_lt_i32_e64 s[62:63], 0, v121
	v_cmp_lt_i32_e64 s[64:65], 0, v122
	v_cmp_lt_i32_e64 s[66:67], 0, v123
	v_max_f32_e32 v24, v24, v28
	v_max_f32_e32 v25, v25, v29
	v_max_f32_e32 v26, v26, v30
	v_max_f32_e32 v27, v27, v31
	v_cndmask_b32_e64 v24, 0, v24, s[60:61]
	v_cndmask_b32_e64 v25, 0, v25, s[62:63]
	v_cndmask_b32_e64 v26, 0, v26, s[64:65]
	v_cndmask_b32_e64 v27, 0, v27, s[66:67]
	v_cvt_pkrtz_f16_f32 v32, v24, v25
	v_cvt_pkrtz_f16_f32 v33, v26, v27
	s_waitcnt lgkmcnt(0)
	v_pk_mul_f32 v[24:25], v[16:17], s[32:33] op_sel:[0,1] op_sel_hi:[1,1]
	v_pk_mul_f32 v[26:27], v[18:19], s[32:33] op_sel:[0,1] op_sel_hi:[1,1]
	v_pk_mul_f32 v[28:29], v[20:21], s[40:41] op_sel:[0,1] op_sel_hi:[1,1]
	v_pk_mul_f32 v[30:31], v[22:23], s[40:41] op_sel:[0,1] op_sel_hi:[1,1]
	v_mfma_f32_32x32x16_f16 v[40:55], v[184:187], v[200:203], v[40:55]
	v_cmp_lt_i32_e64 s[60:61], 0, v124
	v_cmp_lt_i32_e64 s[62:63], 0, v125
	v_cmp_lt_i32_e64 s[64:65], 0, v126
	v_cmp_lt_i32_e64 s[66:67], 0, v127
	v_max_f32_e32 v24, v24, v28
	v_max_f32_e32 v25, v25, v29
	v_max_f32_e32 v26, v26, v30
	v_max_f32_e32 v27, v27, v31
	v_cndmask_b32_e64 v24, 0, v24, s[60:61]
	v_cndmask_b32_e64 v25, 0, v25, s[62:63]
	v_cndmask_b32_e64 v26, 0, v26, s[64:65]
	v_cndmask_b32_e64 v27, 0, v27, s[66:67]
	v_mfma_f32_32x32x16_f16 v[56:71], v[184:187], v[204:207], v[56:71]
	v_cvt_pkrtz_f16_f32 v34, v24, v25
	v_cvt_pkrtz_f16_f32 v35, v26, v27
	ds_write2_b64 v5, v[32:33], v[34:35] offset0:0 offset1:66
	v_pk_mul_f32 v[24:25], v[16:17], s[34:35] op_sel_hi:[1,0]
	v_pk_mul_f32 v[26:27], v[18:19], s[34:35] op_sel_hi:[1,0]
	v_pk_mul_f32 v[28:29], v[20:21], s[42:43] op_sel_hi:[1,0]
	v_pk_mul_f32 v[30:31], v[22:23], s[42:43] op_sel_hi:[1,0]
	v_mfma_f32_32x32x16_f16 v[72:87], v[184:187], v[12:15], v[72:87]
	v_cmp_lt_i32_e64 s[60:61], 0, v128
	v_cmp_lt_i32_e64 s[62:63], 0, v129
	v_cmp_lt_i32_e64 s[64:65], 0, v130
	v_cmp_lt_i32_e64 s[66:67], 0, v131
	v_max_f32_e32 v24, v24, v28
	v_max_f32_e32 v25, v25, v29
	v_max_f32_e32 v26, v26, v30
	v_max_f32_e32 v27, v27, v31
	v_cndmask_b32_e64 v24, 0, v24, s[60:61]
	v_cndmask_b32_e64 v25, 0, v25, s[62:63]
	v_cndmask_b32_e64 v26, 0, v26, s[64:65]
	v_cndmask_b32_e64 v27, 0, v27, s[66:67]
	v_mfma_f32_32x32x16_f16 v[40:55], v[188:191], v[208:211], v[40:55]
	v_cvt_pkrtz_f16_f32 v32, v24, v25
	v_cvt_pkrtz_f16_f32 v33, v26, v27
	v_pk_mul_f32 v[24:25], v[16:17], s[34:35] op_sel:[0,1] op_sel_hi:[1,1]
	v_pk_mul_f32 v[26:27], v[18:19], s[34:35] op_sel:[0,1] op_sel_hi:[1,1]
	v_pk_mul_f32 v[28:29], v[20:21], s[42:43] op_sel:[0,1] op_sel_hi:[1,1]
	v_pk_mul_f32 v[30:31], v[22:23], s[42:43] op_sel:[0,1] op_sel_hi:[1,1]
	v_mfma_f32_32x32x16_f16 v[56:71], v[188:191], v[212:215], v[56:71]
	v_cmp_lt_i32_e64 s[60:61], 0, v132
	v_cmp_lt_i32_e64 s[62:63], 0, v133
	v_cmp_lt_i32_e64 s[64:65], 0, v134
	v_cmp_lt_i32_e64 s[66:67], 0, v135
	v_max_f32_e32 v24, v24, v28
	v_max_f32_e32 v25, v25, v29
	v_max_f32_e32 v26, v26, v30
	v_max_f32_e32 v27, v27, v31
	v_cndmask_b32_e64 v24, 0, v24, s[60:61]
	v_cndmask_b32_e64 v25, 0, v25, s[62:63]
	v_cndmask_b32_e64 v26, 0, v26, s[64:65]
	v_cndmask_b32_e64 v27, 0, v27, s[66:67]
	v_mfma_f32_32x32x16_f16 v[72:87], v[188:191], v[12:15], v[72:87]
	v_cvt_pkrtz_f16_f32 v34, v24, v25
	v_cvt_pkrtz_f16_f32 v35, v26, v27
	ds_write2_b64 v5, v[32:33], v[34:35] offset0:132 offset1:198
	v_pk_mul_f32 v[24:25], v[16:17], s[36:37] op_sel_hi:[1,0]
	v_pk_mul_f32 v[26:27], v[18:19], s[36:37] op_sel_hi:[1,0]
	v_pk_mul_f32 v[28:29], v[20:21], s[44:45] op_sel_hi:[1,0]
	v_pk_mul_f32 v[30:31], v[22:23], s[44:45] op_sel_hi:[1,0]
	v_mfma_f32_32x32x16_f16 v[40:55], v[192:195], v[216:219], v[40:55]
	v_cmp_lt_i32_e64 s[60:61], 0, v136
	v_cmp_lt_i32_e64 s[62:63], 0, v137
	v_cmp_lt_i32_e64 s[64:65], 0, v138
	v_cmp_lt_i32_e64 s[66:67], 0, v139
	v_max_f32_e32 v24, v24, v28
	v_max_f32_e32 v25, v25, v29
	v_max_f32_e32 v26, v26, v30
	v_max_f32_e32 v27, v27, v31
	v_cndmask_b32_e64 v24, 0, v24, s[60:61]
	v_cndmask_b32_e64 v25, 0, v25, s[62:63]
	v_cndmask_b32_e64 v26, 0, v26, s[64:65]
	v_cndmask_b32_e64 v27, 0, v27, s[66:67]
	v_mfma_f32_32x32x16_f16 v[56:71], v[192:195], v[220:223], v[56:71]
	v_cvt_pkrtz_f16_f32 v32, v24, v25
	v_cvt_pkrtz_f16_f32 v33, v26, v27
	v_pk_mul_f32 v[24:25], v[16:17], s[36:37] op_sel:[0,1] op_sel_hi:[1,1]
	v_pk_mul_f32 v[26:27], v[18:19], s[36:37] op_sel:[0,1] op_sel_hi:[1,1]
	v_pk_mul_f32 v[28:29], v[20:21], s[44:45] op_sel:[0,1] op_sel_hi:[1,1]
	v_pk_mul_f32 v[30:31], v[22:23], s[44:45] op_sel:[0,1] op_sel_hi:[1,1]
	v_mfma_f32_32x32x16_f16 v[72:87], v[192:195], v[12:15], v[72:87]
	v_cmp_lt_i32_e64 s[60:61], 0, v140
	v_cmp_lt_i32_e64 s[62:63], 0, v141
	v_cmp_lt_i32_e64 s[64:65], 0, v142
	v_cmp_lt_i32_e64 s[66:67], 0, v143
	v_max_f32_e32 v24, v24, v28
	v_max_f32_e32 v25, v25, v29
	v_max_f32_e32 v26, v26, v30
	v_max_f32_e32 v27, v27, v31
	v_cndmask_b32_e64 v24, 0, v24, s[60:61]
	v_cndmask_b32_e64 v25, 0, v25, s[62:63]
	v_cndmask_b32_e64 v26, 0, v26, s[64:65]
	v_cndmask_b32_e64 v27, 0, v27, s[66:67]
	v_mfma_f32_32x32x16_f16 v[40:55], v[196:199], v[224:227], v[40:55]
	v_cvt_pkrtz_f16_f32 v34, v24, v25
	v_cvt_pkrtz_f16_f32 v35, v26, v27
	ds_write2_b64 v6, v[32:33], v[34:35] offset0:0 offset1:66
	v_pk_mul_f32 v[24:25], v[16:17], s[38:39] op_sel_hi:[1,0]
	v_pk_mul_f32 v[26:27], v[18:19], s[38:39] op_sel_hi:[1,0]
	v_pk_mul_f32 v[28:29], v[20:21], s[46:47] op_sel_hi:[1,0]
	v_pk_mul_f32 v[30:31], v[22:23], s[46:47] op_sel_hi:[1,0]
	v_mfma_f32_32x32x16_f16 v[56:71], v[196:199], v[228:231], v[56:71]
	v_cmp_lt_i32_e64 s[60:61], 0, v144
	v_cmp_lt_i32_e64 s[62:63], 0, v145
	v_cmp_lt_i32_e64 s[64:65], 0, v146
	v_cmp_lt_i32_e64 s[66:67], 0, v147
	v_max_f32_e32 v24, v24, v28
	v_max_f32_e32 v25, v25, v29
	v_max_f32_e32 v26, v26, v30
	v_max_f32_e32 v27, v27, v31
	v_cndmask_b32_e64 v24, 0, v24, s[60:61]
	v_cndmask_b32_e64 v25, 0, v25, s[62:63]
	v_cndmask_b32_e64 v26, 0, v26, s[64:65]
	v_cndmask_b32_e64 v27, 0, v27, s[66:67]
	v_cvt_pkrtz_f16_f32 v32, v24, v25
	v_cvt_pkrtz_f16_f32 v33, v26, v27
	v_pk_mul_f32 v[24:25], v[16:17], s[38:39] op_sel:[0,1] op_sel_hi:[1,1]
	v_pk_mul_f32 v[26:27], v[18:19], s[38:39] op_sel:[0,1] op_sel_hi:[1,1]
	v_pk_mul_f32 v[28:29], v[20:21], s[46:47] op_sel:[0,1] op_sel_hi:[1,1]
	v_pk_mul_f32 v[30:31], v[22:23], s[46:47] op_sel:[0,1] op_sel_hi:[1,1]
	v_mfma_f32_32x32x16_f16 v[72:87], v[196:199], v[12:15], v[72:87]
	v_cmp_lt_i32_e64 s[60:61], 0, v148
	v_cmp_lt_i32_e64 s[62:63], 0, v149
	v_cmp_lt_i32_e64 s[64:65], 0, v150
	v_cmp_lt_i32_e64 s[66:67], 0, v151
	v_max_f32_e32 v24, v24, v28
	v_max_f32_e32 v25, v25, v29
	v_max_f32_e32 v26, v26, v30
	v_max_f32_e32 v27, v27, v31
	v_cndmask_b32_e64 v24, 0, v24, s[60:61]
	v_cndmask_b32_e64 v25, 0, v25, s[62:63]
	v_cndmask_b32_e64 v26, 0, v26, s[64:65]
	v_cndmask_b32_e64 v27, 0, v27, s[66:67]
	v_cvt_pkrtz_f16_f32 v34, v24, v25
	v_cvt_pkrtz_f16_f32 v35, v26, v27
	ds_write2_b64 v6, v[32:33], v[34:35] offset0:132 offset1:198
	ds_write_b128 v9, v[168:171] offset:32768
	ds_write_b128 v9, v[172:175] offset:33792
	ds_write_b128 v9, v[176:179] offset:34816
	ds_write_b128 v9, v[180:183] offset:35840
	s_add_u32 s3, s19, 4
	s_and_b32 s3, s3, 7
	s_lshl_b32 s3, s3, 10
	v_add_u32_e32 v11, s3, v10
	ds_read_b128 v[16:19], v11
	ds_read_b128 v[20:23], v11 offset:8192
	s_waitcnt lgkmcnt(0)
	s_barrier
	ds_read_b128 v[184:187], v7 offset:33792
	ds_read_b128 v[200:203], v8 offset:32768
	ds_read_b128 v[204:207], v8 offset:33792
	ds_read_b128 v[188:191], v7 offset:33824
	ds_read_b128 v[208:211], v8 offset:34816
	ds_read_b128 v[212:215], v8 offset:35840
	ds_read_b128 v[192:195], v7 offset:33856
	ds_read_b128 v[216:219], v8 offset:36864
	ds_read_b128 v[220:223], v8 offset:37888
	ds_read_b128 v[196:199], v7 offset:33888
	ds_read_b128 v[224:227], v8 offset:38912
	ds_read_b128 v[228:231], v8 offset:39936
	s_add_u32 s3, s19, 5
	s_and_b32 s3, s3, 7
	s_lshl_b32 s57, s3, 10
	s_add_u32 s48, s57, s22
	s_add_u32 s49, s48, 0x2000
	s_add_u32 s50, s48, 0x4000
	s_add_u32 s51, s48, 0x6000
	s_add_u32 s52, s48, 0x8000
	s_add_u32 s53, s48, 0xa000
	s_add_u32 s54, s48, 0xc000
	s_add_u32 s55, s48, 0xe000
	s_lshl_b32 s56, s3, 15
	s_add_u32 s56, s56, s23
	buffer_load_dwordx4 v[120:123], v1, s[4:7], s48 offen nt
	buffer_load_dwordx4 v[124:127], v1, s[4:7], s49 offen nt
	buffer_load_dwordx4 v[128:131], v1, s[4:7], s50 offen nt
	buffer_load_dwordx4 v[132:135], v1, s[4:7], s51 offen nt
	buffer_load_dwordx4 v[136:139], v1, s[4:7], s52 offen nt
	buffer_load_dwordx4 v[140:143], v1, s[4:7], s53 offen nt
	buffer_load_dwordx4 v[144:147], v1, s[4:7], s54 offen nt
	buffer_load_dwordx4 v[148:151], v1, s[4:7], s55 offen nt
	buffer_load_dwordx4 v[168:171], v1, s[8:11], s56 offen
	buffer_load_dwordx4 v[172:175], v1, s[8:11], s56 offen offset:1024
	buffer_load_dwordx4 v[176:179], v1, s[8:11], s56 offen offset:2048
	buffer_load_dwordx4 v[180:183], v1, s[8:11], s56 offen offset:3072
	s_waitcnt vmcnt(12)
	v_pk_mul_f32 v[24:25], v[16:17], s[32:33] op_sel_hi:[1,0]
	v_pk_mul_f32 v[26:27], v[18:19], s[32:33] op_sel_hi:[1,0]
	v_pk_mul_f32 v[28:29], v[20:21], s[40:41] op_sel_hi:[1,0]
	v_pk_mul_f32 v[30:31], v[22:23], s[40:41] op_sel_hi:[1,0]
	v_cmp_lt_i32_e64 s[60:61], 0, v88
	v_cmp_lt_i32_e64 s[62:63], 0, v89
	v_cmp_lt_i32_e64 s[64:65], 0, v90
	v_cmp_lt_i32_e64 s[66:67], 0, v91
	v_max_f32_e32 v24, v24, v28
	v_max_f32_e32 v25, v25, v29
	v_max_f32_e32 v26, v26, v30
	v_max_f32_e32 v27, v27, v31
	v_cndmask_b32_e64 v24, 0, v24, s[60:61]
	v_cndmask_b32_e64 v25, 0, v25, s[62:63]
	v_cndmask_b32_e64 v26, 0, v26, s[64:65]
	v_cndmask_b32_e64 v27, 0, v27, s[66:67]
	v_cvt_pkrtz_f16_f32 v32, v24, v25
	v_cvt_pkrtz_f16_f32 v33, v26, v27
	s_waitcnt lgkmcnt(0)
	v_pk_mul_f32 v[24:25], v[16:17], s[32:33] op_sel:[0,1] op_sel_hi:[1,1]
	v_pk_mul_f32 v[26:27], v[18:19], s[32:33] op_sel:[0,1] op_sel_hi:[1,1]
	v_pk_mul_f32 v[28:29], v[20:21], s[40:41] op_sel:[0,1] op_sel_hi:[1,1]
	v_pk_mul_f32 v[30:31], v[22:23], s[40:41] op_sel:[0,1] op_sel_hi:[1,1]
	v_mfma_f32_32x32x16_f16 v[40:55], v[184:187], v[200:203], v[40:55]
	v_cmp_lt_i32_e64 s[60:61], 0, v92
	v_cmp_lt_i32_e64 s[62:63], 0, v93
	v_cmp_lt_i32_e64 s[64:65], 0, v94
	v_cmp_lt_i32_e64 s[66:67], 0, v95
	v_max_f32_e32 v24, v24, v28
	v_max_f32_e32 v25, v25, v29
	v_max_f32_e32 v26, v26, v30
	v_max_f32_e32 v27, v27, v31
	v_cndmask_b32_e64 v24, 0, v24, s[60:61]
	v_cndmask_b32_e64 v25, 0, v25, s[62:63]
	v_cndmask_b32_e64 v26, 0, v26, s[64:65]
	v_cndmask_b32_e64 v27, 0, v27, s[66:67]
	v_mfma_f32_32x32x16_f16 v[56:71], v[184:187], v[204:207], v[56:71]
	v_cvt_pkrtz_f16_f32 v34, v24, v25
	v_cvt_pkrtz_f16_f32 v35, v26, v27
	ds_write2_b64 v3, v[32:33], v[34:35] offset0:0 offset1:66
	v_pk_mul_f32 v[24:25], v[16:17], s[34:35] op_sel_hi:[1,0]
	v_pk_mul_f32 v[26:27], v[18:19], s[34:35] op_sel_hi:[1,0]
	v_pk_mul_f32 v[28:29], v[20:21], s[42:43] op_sel_hi:[1,0]
	v_pk_mul_f32 v[30:31], v[22:23], s[42:43] op_sel_hi:[1,0]
	v_mfma_f32_32x32x16_f16 v[72:87], v[184:187], v[12:15], v[72:87]
	v_cmp_lt_i32_e64 s[60:61], 0, v96
	v_cmp_lt_i32_e64 s[62:63], 0, v97
	v_cmp_lt_i32_e64 s[64:65], 0, v98
	v_cmp_lt_i32_e64 s[66:67], 0, v99
	v_max_f32_e32 v24, v24, v28
	v_max_f32_e32 v25, v25, v29
	v_max_f32_e32 v26, v26, v30
	v_max_f32_e32 v27, v27, v31
	v_cndmask_b32_e64 v24, 0, v24, s[60:61]
	v_cndmask_b32_e64 v25, 0, v25, s[62:63]
	v_cndmask_b32_e64 v26, 0, v26, s[64:65]
	v_cndmask_b32_e64 v27, 0, v27, s[66:67]
	v_mfma_f32_32x32x16_f16 v[40:55], v[188:191], v[208:211], v[40:55]
	v_cvt_pkrtz_f16_f32 v32, v24, v25
	v_cvt_pkrtz_f16_f32 v33, v26, v27
	v_pk_mul_f32 v[24:25], v[16:17], s[34:35] op_sel:[0,1] op_sel_hi:[1,1]
	v_pk_mul_f32 v[26:27], v[18:19], s[34:35] op_sel:[0,1] op_sel_hi:[1,1]
	v_pk_mul_f32 v[28:29], v[20:21], s[42:43] op_sel:[0,1] op_sel_hi:[1,1]
	v_pk_mul_f32 v[30:31], v[22:23], s[42:43] op_sel:[0,1] op_sel_hi:[1,1]
	v_mfma_f32_32x32x16_f16 v[56:71], v[188:191], v[212:215], v[56:71]
	v_cmp_lt_i32_e64 s[60:61], 0, v100
	v_cmp_lt_i32_e64 s[62:63], 0, v101
	v_cmp_lt_i32_e64 s[64:65], 0, v102
	v_cmp_lt_i32_e64 s[66:67], 0, v103
	v_max_f32_e32 v24, v24, v28
	v_max_f32_e32 v25, v25, v29
	v_max_f32_e32 v26, v26, v30
	v_max_f32_e32 v27, v27, v31
	v_cndmask_b32_e64 v24, 0, v24, s[60:61]
	v_cndmask_b32_e64 v25, 0, v25, s[62:63]
	v_cndmask_b32_e64 v26, 0, v26, s[64:65]
	v_cndmask_b32_e64 v27, 0, v27, s[66:67]
	v_mfma_f32_32x32x16_f16 v[72:87], v[188:191], v[12:15], v[72:87]
	v_cvt_pkrtz_f16_f32 v34, v24, v25
	v_cvt_pkrtz_f16_f32 v35, v26, v27
	ds_write2_b64 v3, v[32:33], v[34:35] offset0:132 offset1:198
	v_pk_mul_f32 v[24:25], v[16:17], s[36:37] op_sel_hi:[1,0]
	v_pk_mul_f32 v[26:27], v[18:19], s[36:37] op_sel_hi:[1,0]
	v_pk_mul_f32 v[28:29], v[20:21], s[44:45] op_sel_hi:[1,0]
	v_pk_mul_f32 v[30:31], v[22:23], s[44:45] op_sel_hi:[1,0]
	v_mfma_f32_32x32x16_f16 v[40:55], v[192:195], v[216:219], v[40:55]
	v_cmp_lt_i32_e64 s[60:61], 0, v104
	v_cmp_lt_i32_e64 s[62:63], 0, v105
	v_cmp_lt_i32_e64 s[64:65], 0, v106
	v_cmp_lt_i32_e64 s[66:67], 0, v107
	v_max_f32_e32 v24, v24, v28
	v_max_f32_e32 v25, v25, v29
	v_max_f32_e32 v26, v26, v30
	v_max_f32_e32 v27, v27, v31
	v_cndmask_b32_e64 v24, 0, v24, s[60:61]
	v_cndmask_b32_e64 v25, 0, v25, s[62:63]
	v_cndmask_b32_e64 v26, 0, v26, s[64:65]
	v_cndmask_b32_e64 v27, 0, v27, s[66:67]
	v_mfma_f32_32x32x16_f16 v[56:71], v[192:195], v[220:223], v[56:71]
	v_cvt_pkrtz_f16_f32 v32, v24, v25
	v_cvt_pkrtz_f16_f32 v33, v26, v27
	v_pk_mul_f32 v[24:25], v[16:17], s[36:37] op_sel:[0,1] op_sel_hi:[1,1]
	v_pk_mul_f32 v[26:27], v[18:19], s[36:37] op_sel:[0,1] op_sel_hi:[1,1]
	v_pk_mul_f32 v[28:29], v[20:21], s[44:45] op_sel:[0,1] op_sel_hi:[1,1]
	v_pk_mul_f32 v[30:31], v[22:23], s[44:45] op_sel:[0,1] op_sel_hi:[1,1]
	v_mfma_f32_32x32x16_f16 v[72:87], v[192:195], v[12:15], v[72:87]
	v_cmp_lt_i32_e64 s[60:61], 0, v108
	v_cmp_lt_i32_e64 s[62:63], 0, v109
	v_cmp_lt_i32_e64 s[64:65], 0, v110
	v_cmp_lt_i32_e64 s[66:67], 0, v111
	v_max_f32_e32 v24, v24, v28
	v_max_f32_e32 v25, v25, v29
	v_max_f32_e32 v26, v26, v30
	v_max_f32_e32 v27, v27, v31
	v_cndmask_b32_e64 v24, 0, v24, s[60:61]
	v_cndmask_b32_e64 v25, 0, v25, s[62:63]
	v_cndmask_b32_e64 v26, 0, v26, s[64:65]
	v_cndmask_b32_e64 v27, 0, v27, s[66:67]
	v_mfma_f32_32x32x16_f16 v[40:55], v[196:199], v[224:227], v[40:55]
	v_cvt_pkrtz_f16_f32 v34, v24, v25
	v_cvt_pkrtz_f16_f32 v35, v26, v27
	ds_write2_b64 v4, v[32:33], v[34:35] offset0:0 offset1:66
	v_pk_mul_f32 v[24:25], v[16:17], s[38:39] op_sel_hi:[1,0]
	v_pk_mul_f32 v[26:27], v[18:19], s[38:39] op_sel_hi:[1,0]
	v_pk_mul_f32 v[28:29], v[20:21], s[46:47] op_sel_hi:[1,0]
	v_pk_mul_f32 v[30:31], v[22:23], s[46:47] op_sel_hi:[1,0]
	v_mfma_f32_32x32x16_f16 v[56:71], v[196:199], v[228:231], v[56:71]
	v_cmp_lt_i32_e64 s[60:61], 0, v112
	v_cmp_lt_i32_e64 s[62:63], 0, v113
	v_cmp_lt_i32_e64 s[64:65], 0, v114
	v_cmp_lt_i32_e64 s[66:67], 0, v115
	v_max_f32_e32 v24, v24, v28
	v_max_f32_e32 v25, v25, v29
	v_max_f32_e32 v26, v26, v30
	v_max_f32_e32 v27, v27, v31
	v_cndmask_b32_e64 v24, 0, v24, s[60:61]
	v_cndmask_b32_e64 v25, 0, v25, s[62:63]
	v_cndmask_b32_e64 v26, 0, v26, s[64:65]
	v_cndmask_b32_e64 v27, 0, v27, s[66:67]
	v_cvt_pkrtz_f16_f32 v32, v24, v25
	v_cvt_pkrtz_f16_f32 v33, v26, v27
	v_pk_mul_f32 v[24:25], v[16:17], s[38:39] op_sel:[0,1] op_sel_hi:[1,1]
	v_pk_mul_f32 v[26:27], v[18:19], s[38:39] op_sel:[0,1] op_sel_hi:[1,1]
	v_pk_mul_f32 v[28:29], v[20:21], s[46:47] op_sel:[0,1] op_sel_hi:[1,1]
	v_pk_mul_f32 v[30:31], v[22:23], s[46:47] op_sel:[0,1] op_sel_hi:[1,1]
	v_mfma_f32_32x32x16_f16 v[72:87], v[196:199], v[12:15], v[72:87]
	v_cmp_lt_i32_e64 s[60:61], 0, v116
	v_cmp_lt_i32_e64 s[62:63], 0, v117
	v_cmp_lt_i32_e64 s[64:65], 0, v118
	v_cmp_lt_i32_e64 s[66:67], 0, v119
	v_max_f32_e32 v24, v24, v28
	v_max_f32_e32 v25, v25, v29
	v_max_f32_e32 v26, v26, v30
	v_max_f32_e32 v27, v27, v31
	v_cndmask_b32_e64 v24, 0, v24, s[60:61]
	v_cndmask_b32_e64 v25, 0, v25, s[62:63]
	v_cndmask_b32_e64 v26, 0, v26, s[64:65]
	v_cndmask_b32_e64 v27, 0, v27, s[66:67]
	v_cvt_pkrtz_f16_f32 v34, v24, v25
	v_cvt_pkrtz_f16_f32 v35, v26, v27
	ds_write2_b64 v4, v[32:33], v[34:35] offset0:132 offset1:198
	ds_write_b128 v9, v[152:155] offset:0
	ds_write_b128 v9, v[156:159] offset:1024
	ds_write_b128 v9, v[160:163] offset:2048
	ds_write_b128 v9, v[164:167] offset:3072
	s_add_u32 s3, s19, 5
	s_and_b32 s3, s3, 7
	s_lshl_b32 s3, s3, 10
	v_add_u32_e32 v11, s3, v10
	ds_read_b128 v[16:19], v11
	ds_read_b128 v[20:23], v11 offset:8192
	s_waitcnt lgkmcnt(0)
	s_barrier
	ds_read_b128 v[184:187], v7 offset:0
	ds_read_b128 v[200:203], v8 offset:0
	ds_read_b128 v[204:207], v8 offset:1024
	ds_read_b128 v[188:191], v7 offset:32
	ds_read_b128 v[208:211], v8 offset:2048
	ds_read_b128 v[212:215], v8 offset:3072
	ds_read_b128 v[192:195], v7 offset:64
	ds_read_b128 v[216:219], v8 offset:4096
	ds_read_b128 v[220:223], v8 offset:5120
	ds_read_b128 v[196:199], v7 offset:96
	ds_read_b128 v[224:227], v8 offset:6144
	ds_read_b128 v[228:231], v8 offset:7168
	s_add_u32 s3, s19, 6
	s_and_b32 s3, s3, 7
	s_lshl_b32 s57, s3, 10
	s_add_u32 s48, s57, s22
	s_add_u32 s49, s48, 0x2000
	s_add_u32 s50, s48, 0x4000
	s_add_u32 s51, s48, 0x6000
	s_add_u32 s52, s48, 0x8000
	s_add_u32 s53, s48, 0xa000
	s_add_u32 s54, s48, 0xc000
	s_add_u32 s55, s48, 0xe000
	s_lshl_b32 s56, s3, 15
	s_add_u32 s56, s56, s23
	buffer_load_dwordx4 v[88:91], v1, s[4:7], s48 offen nt
	buffer_load_dwordx4 v[92:95], v1, s[4:7], s49 offen nt
	buffer_load_dwordx4 v[96:99], v1, s[4:7], s50 offen nt
	buffer_load_dwordx4 v[100:103], v1, s[4:7], s51 offen nt
	buffer_load_dwordx4 v[104:107], v1, s[4:7], s52 offen nt
	buffer_load_dwordx4 v[108:111], v1, s[4:7], s53 offen nt
	buffer_load_dwordx4 v[112:115], v1, s[4:7], s54 offen nt
	buffer_load_dwordx4 v[116:119], v1, s[4:7], s55 offen nt
	buffer_load_dwordx4 v[152:155], v1, s[8:11], s56 offen
	buffer_load_dwordx4 v[156:159], v1, s[8:11], s56 offen offset:1024
	buffer_load_dwordx4 v[160:163], v1, s[8:11], s56 offen offset:2048
	buffer_load_dwordx4 v[164:167], v1, s[8:11], s56 offen offset:3072
	s_waitcnt vmcnt(12)
	v_pk_mul_f32 v[24:25], v[16:17], s[32:33] op_sel_hi:[1,0]
	v_pk_mul_f32 v[26:27], v[18:19], s[32:33] op_sel_hi:[1,0]
	v_pk_mul_f32 v[28:29], v[20:21], s[40:41] op_sel_hi:[1,0]
	v_pk_mul_f32 v[30:31], v[22:23], s[40:41] op_sel_hi:[1,0]
	v_cmp_lt_i32_e64 s[60:61], 0, v120
	v_cmp_lt_i32_e64 s[62:63], 0, v121
	v_cmp_lt_i32_e64 s[64:65], 0, v122
	v_cmp_lt_i32_e64 s[66:67], 0, v123
	v_max_f32_e32 v24, v24, v28
	v_max_f32_e32 v25, v25, v29
	v_max_f32_e32 v26, v26, v30
	v_max_f32_e32 v27, v27, v31
	v_cndmask_b32_e64 v24, 0, v24, s[60:61]
	v_cndmask_b32_e64 v25, 0, v25, s[62:63]
	v_cndmask_b32_e64 v26, 0, v26, s[64:65]
	v_cndmask_b32_e64 v27, 0, v27, s[66:67]
	v_cvt_pkrtz_f16_f32 v32, v24, v25
	v_cvt_pkrtz_f16_f32 v33, v26, v27
	s_waitcnt lgkmcnt(0)
	v_pk_mul_f32 v[24:25], v[16:17], s[32:33] op_sel:[0,1] op_sel_hi:[1,1]
	v_pk_mul_f32 v[26:27], v[18:19], s[32:33] op_sel:[0,1] op_sel_hi:[1,1]
	v_pk_mul_f32 v[28:29], v[20:21], s[40:41] op_sel:[0,1] op_sel_hi:[1,1]
	v_pk_mul_f32 v[30:31], v[22:23], s[40:41] op_sel:[0,1] op_sel_hi:[1,1]
	v_mfma_f32_32x32x16_f16 v[40:55], v[184:187], v[200:203], v[40:55]
	v_cmp_lt_i32_e64 s[60:61], 0, v124
	v_cmp_lt_i32_e64 s[62:63], 0, v125
	v_cmp_lt_i32_e64 s[64:65], 0, v126
	v_cmp_lt_i32_e64 s[66:67], 0, v127
	v_max_f32_e32 v24, v24, v28
	v_max_f32_e32 v25, v25, v29
	v_max_f32_e32 v26, v26, v30
	v_max_f32_e32 v27, v27, v31
	v_cndmask_b32_e64 v24, 0, v24, s[60:61]
	v_cndmask_b32_e64 v25, 0, v25, s[62:63]
	v_cndmask_b32_e64 v26, 0, v26, s[64:65]
	v_cndmask_b32_e64 v27, 0, v27, s[66:67]
	v_mfma_f32_32x32x16_f16 v[56:71], v[184:187], v[204:207], v[56:71]
	v_cvt_pkrtz_f16_f32 v34, v24, v25
	v_cvt_pkrtz_f16_f32 v35, v26, v27
	ds_write2_b64 v5, v[32:33], v[34:35] offset0:0 offset1:66
	v_pk_mul_f32 v[24:25], v[16:17], s[34:35] op_sel_hi:[1,0]
	v_pk_mul_f32 v[26:27], v[18:19], s[34:35] op_sel_hi:[1,0]
	v_pk_mul_f32 v[28:29], v[20:21], s[42:43] op_sel_hi:[1,0]
	v_pk_mul_f32 v[30:31], v[22:23], s[42:43] op_sel_hi:[1,0]
	v_mfma_f32_32x32x16_f16 v[72:87], v[184:187], v[12:15], v[72:87]
	v_cmp_lt_i32_e64 s[60:61], 0, v128
	v_cmp_lt_i32_e64 s[62:63], 0, v129
	v_cmp_lt_i32_e64 s[64:65], 0, v130
	v_cmp_lt_i32_e64 s[66:67], 0, v131
	v_max_f32_e32 v24, v24, v28
	v_max_f32_e32 v25, v25, v29
	v_max_f32_e32 v26, v26, v30
	v_max_f32_e32 v27, v27, v31
	v_cndmask_b32_e64 v24, 0, v24, s[60:61]
	v_cndmask_b32_e64 v25, 0, v25, s[62:63]
	v_cndmask_b32_e64 v26, 0, v26, s[64:65]
	v_cndmask_b32_e64 v27, 0, v27, s[66:67]
	v_mfma_f32_32x32x16_f16 v[40:55], v[188:191], v[208:211], v[40:55]
	v_cvt_pkrtz_f16_f32 v32, v24, v25
	v_cvt_pkrtz_f16_f32 v33, v26, v27
	v_pk_mul_f32 v[24:25], v[16:17], s[34:35] op_sel:[0,1] op_sel_hi:[1,1]
	v_pk_mul_f32 v[26:27], v[18:19], s[34:35] op_sel:[0,1] op_sel_hi:[1,1]
	v_pk_mul_f32 v[28:29], v[20:21], s[42:43] op_sel:[0,1] op_sel_hi:[1,1]
	v_pk_mul_f32 v[30:31], v[22:23], s[42:43] op_sel:[0,1] op_sel_hi:[1,1]
	v_mfma_f32_32x32x16_f16 v[56:71], v[188:191], v[212:215], v[56:71]
	v_cmp_lt_i32_e64 s[60:61], 0, v132
	v_cmp_lt_i32_e64 s[62:63], 0, v133
	v_cmp_lt_i32_e64 s[64:65], 0, v134
	v_cmp_lt_i32_e64 s[66:67], 0, v135
	v_max_f32_e32 v24, v24, v28
	v_max_f32_e32 v25, v25, v29
	v_max_f32_e32 v26, v26, v30
	v_max_f32_e32 v27, v27, v31
	v_cndmask_b32_e64 v24, 0, v24, s[60:61]
	v_cndmask_b32_e64 v25, 0, v25, s[62:63]
	v_cndmask_b32_e64 v26, 0, v26, s[64:65]
	v_cndmask_b32_e64 v27, 0, v27, s[66:67]
	v_mfma_f32_32x32x16_f16 v[72:87], v[188:191], v[12:15], v[72:87]
	v_cvt_pkrtz_f16_f32 v34, v24, v25
	v_cvt_pkrtz_f16_f32 v35, v26, v27
	ds_write2_b64 v5, v[32:33], v[34:35] offset0:132 offset1:198
	v_pk_mul_f32 v[24:25], v[16:17], s[36:37] op_sel_hi:[1,0]
	v_pk_mul_f32 v[26:27], v[18:19], s[36:37] op_sel_hi:[1,0]
	v_pk_mul_f32 v[28:29], v[20:21], s[44:45] op_sel_hi:[1,0]
	v_pk_mul_f32 v[30:31], v[22:23], s[44:45] op_sel_hi:[1,0]
	v_mfma_f32_32x32x16_f16 v[40:55], v[192:195], v[216:219], v[40:55]
	v_cmp_lt_i32_e64 s[60:61], 0, v136
	v_cmp_lt_i32_e64 s[62:63], 0, v137
	v_cmp_lt_i32_e64 s[64:65], 0, v138
	v_cmp_lt_i32_e64 s[66:67], 0, v139
	v_max_f32_e32 v24, v24, v28
	v_max_f32_e32 v25, v25, v29
	v_max_f32_e32 v26, v26, v30
	v_max_f32_e32 v27, v27, v31
	v_cndmask_b32_e64 v24, 0, v24, s[60:61]
	v_cndmask_b32_e64 v25, 0, v25, s[62:63]
	v_cndmask_b32_e64 v26, 0, v26, s[64:65]
	v_cndmask_b32_e64 v27, 0, v27, s[66:67]
	v_mfma_f32_32x32x16_f16 v[56:71], v[192:195], v[220:223], v[56:71]
	v_cvt_pkrtz_f16_f32 v32, v24, v25
	v_cvt_pkrtz_f16_f32 v33, v26, v27
	v_pk_mul_f32 v[24:25], v[16:17], s[36:37] op_sel:[0,1] op_sel_hi:[1,1]
	v_pk_mul_f32 v[26:27], v[18:19], s[36:37] op_sel:[0,1] op_sel_hi:[1,1]
	v_pk_mul_f32 v[28:29], v[20:21], s[44:45] op_sel:[0,1] op_sel_hi:[1,1]
	v_pk_mul_f32 v[30:31], v[22:23], s[44:45] op_sel:[0,1] op_sel_hi:[1,1]
	v_mfma_f32_32x32x16_f16 v[72:87], v[192:195], v[12:15], v[72:87]
	v_cmp_lt_i32_e64 s[60:61], 0, v140
	v_cmp_lt_i32_e64 s[62:63], 0, v141
	v_cmp_lt_i32_e64 s[64:65], 0, v142
	v_cmp_lt_i32_e64 s[66:67], 0, v143
	v_max_f32_e32 v24, v24, v28
	v_max_f32_e32 v25, v25, v29
	v_max_f32_e32 v26, v26, v30
	v_max_f32_e32 v27, v27, v31
	v_cndmask_b32_e64 v24, 0, v24, s[60:61]
	v_cndmask_b32_e64 v25, 0, v25, s[62:63]
	v_cndmask_b32_e64 v26, 0, v26, s[64:65]
	v_cndmask_b32_e64 v27, 0, v27, s[66:67]
	v_mfma_f32_32x32x16_f16 v[40:55], v[196:199], v[224:227], v[40:55]
	v_cvt_pkrtz_f16_f32 v34, v24, v25
	v_cvt_pkrtz_f16_f32 v35, v26, v27
	ds_write2_b64 v6, v[32:33], v[34:35] offset0:0 offset1:66
	v_pk_mul_f32 v[24:25], v[16:17], s[38:39] op_sel_hi:[1,0]
	v_pk_mul_f32 v[26:27], v[18:19], s[38:39] op_sel_hi:[1,0]
	v_pk_mul_f32 v[28:29], v[20:21], s[46:47] op_sel_hi:[1,0]
	v_pk_mul_f32 v[30:31], v[22:23], s[46:47] op_sel_hi:[1,0]
	v_mfma_f32_32x32x16_f16 v[56:71], v[196:199], v[228:231], v[56:71]
	v_cmp_lt_i32_e64 s[60:61], 0, v144
	v_cmp_lt_i32_e64 s[62:63], 0, v145
	v_cmp_lt_i32_e64 s[64:65], 0, v146
	v_cmp_lt_i32_e64 s[66:67], 0, v147
	v_max_f32_e32 v24, v24, v28
	v_max_f32_e32 v25, v25, v29
	v_max_f32_e32 v26, v26, v30
	v_max_f32_e32 v27, v27, v31
	v_cndmask_b32_e64 v24, 0, v24, s[60:61]
	v_cndmask_b32_e64 v25, 0, v25, s[62:63]
	v_cndmask_b32_e64 v26, 0, v26, s[64:65]
	v_cndmask_b32_e64 v27, 0, v27, s[66:67]
	v_cvt_pkrtz_f16_f32 v32, v24, v25
	v_cvt_pkrtz_f16_f32 v33, v26, v27
	v_pk_mul_f32 v[24:25], v[16:17], s[38:39] op_sel:[0,1] op_sel_hi:[1,1]
	v_pk_mul_f32 v[26:27], v[18:19], s[38:39] op_sel:[0,1] op_sel_hi:[1,1]
	v_pk_mul_f32 v[28:29], v[20:21], s[46:47] op_sel:[0,1] op_sel_hi:[1,1]
	v_pk_mul_f32 v[30:31], v[22:23], s[46:47] op_sel:[0,1] op_sel_hi:[1,1]
	v_mfma_f32_32x32x16_f16 v[72:87], v[196:199], v[12:15], v[72:87]
	v_cmp_lt_i32_e64 s[60:61], 0, v148
	v_cmp_lt_i32_e64 s[62:63], 0, v149
	v_cmp_lt_i32_e64 s[64:65], 0, v150
	v_cmp_lt_i32_e64 s[66:67], 0, v151
	v_max_f32_e32 v24, v24, v28
	v_max_f32_e32 v25, v25, v29
	v_max_f32_e32 v26, v26, v30
	v_max_f32_e32 v27, v27, v31
	v_cndmask_b32_e64 v24, 0, v24, s[60:61]
	v_cndmask_b32_e64 v25, 0, v25, s[62:63]
	v_cndmask_b32_e64 v26, 0, v26, s[64:65]
	v_cndmask_b32_e64 v27, 0, v27, s[66:67]
	v_cvt_pkrtz_f16_f32 v34, v24, v25
	v_cvt_pkrtz_f16_f32 v35, v26, v27
	ds_write2_b64 v6, v[32:33], v[34:35] offset0:132 offset1:198
	ds_write_b128 v9, v[168:171] offset:32768
	ds_write_b128 v9, v[172:175] offset:33792
	ds_write_b128 v9, v[176:179] offset:34816
	ds_write_b128 v9, v[180:183] offset:35840
	s_add_u32 s3, s19, 6
	s_and_b32 s3, s3, 7
	s_lshl_b32 s3, s3, 10
	v_add_u32_e32 v11, s3, v10
	ds_read_b128 v[16:19], v11
	ds_read_b128 v[20:23], v11 offset:8192
	s_waitcnt lgkmcnt(0)
	s_barrier
	ds_read_b128 v[184:187], v7 offset:33792
	ds_read_b128 v[200:203], v8 offset:32768
	ds_read_b128 v[204:207], v8 offset:33792
	ds_read_b128 v[188:191], v7 offset:33824
	ds_read_b128 v[208:211], v8 offset:34816
	ds_read_b128 v[212:215], v8 offset:35840
	ds_read_b128 v[192:195], v7 offset:33856
	ds_read_b128 v[216:219], v8 offset:36864
	ds_read_b128 v[220:223], v8 offset:37888
	ds_read_b128 v[196:199], v7 offset:33888
	ds_read_b128 v[224:227], v8 offset:38912
	ds_read_b128 v[228:231], v8 offset:39936
	s_add_u32 s3, s19, 7
	s_and_b32 s3, s3, 7
	s_lshl_b32 s57, s3, 10
	s_add_u32 s48, s57, s22
	s_add_u32 s49, s48, 0x2000
	s_add_u32 s50, s48, 0x4000
	s_add_u32 s51, s48, 0x6000
	s_add_u32 s52, s48, 0x8000
	s_add_u32 s53, s48, 0xa000
	s_add_u32 s54, s48, 0xc000
	s_add_u32 s55, s48, 0xe000
	s_lshl_b32 s56, s3, 15
	s_add_u32 s56, s56, s23
	buffer_load_dwordx4 v[120:123], v1, s[4:7], s48 offen nt
	buffer_load_dwordx4 v[124:127], v1, s[4:7], s49 offen nt
	buffer_load_dwordx4 v[128:131], v1, s[4:7], s50 offen nt
	buffer_load_dwordx4 v[132:135], v1, s[4:7], s51 offen nt
	buffer_load_dwordx4 v[136:139], v1, s[4:7], s52 offen nt
	buffer_load_dwordx4 v[140:143], v1, s[4:7], s53 offen nt
	buffer_load_dwordx4 v[144:147], v1, s[4:7], s54 offen nt
	buffer_load_dwordx4 v[148:151], v1, s[4:7], s55 offen nt
	buffer_load_dwordx4 v[168:171], v1, s[8:11], s56 offen
	buffer_load_dwordx4 v[172:175], v1, s[8:11], s56 offen offset:1024
	buffer_load_dwordx4 v[176:179], v1, s[8:11], s56 offen offset:2048
	buffer_load_dwordx4 v[180:183], v1, s[8:11], s56 offen offset:3072
	s_waitcnt vmcnt(12)
	v_pk_mul_f32 v[24:25], v[16:17], s[32:33] op_sel_hi:[1,0]
	v_pk_mul_f32 v[26:27], v[18:19], s[32:33] op_sel_hi:[1,0]
	v_pk_mul_f32 v[28:29], v[20:21], s[40:41] op_sel_hi:[1,0]
	v_pk_mul_f32 v[30:31], v[22:23], s[40:41] op_sel_hi:[1,0]
	v_cmp_lt_i32_e64 s[60:61], 0, v88
	v_cmp_lt_i32_e64 s[62:63], 0, v89
	v_cmp_lt_i32_e64 s[64:65], 0, v90
	v_cmp_lt_i32_e64 s[66:67], 0, v91
	v_max_f32_e32 v24, v24, v28
	v_max_f32_e32 v25, v25, v29
	v_max_f32_e32 v26, v26, v30
	v_max_f32_e32 v27, v27, v31
	v_cndmask_b32_e64 v24, 0, v24, s[60:61]
	v_cndmask_b32_e64 v25, 0, v25, s[62:63]
	v_cndmask_b32_e64 v26, 0, v26, s[64:65]
	v_cndmask_b32_e64 v27, 0, v27, s[66:67]
	v_cvt_pkrtz_f16_f32 v32, v24, v25
	v_cvt_pkrtz_f16_f32 v33, v26, v27
	s_waitcnt lgkmcnt(0)
	v_pk_mul_f32 v[24:25], v[16:17], s[32:33] op_sel:[0,1] op_sel_hi:[1,1]
	v_pk_mul_f32 v[26:27], v[18:19], s[32:33] op_sel:[0,1] op_sel_hi:[1,1]
	v_pk_mul_f32 v[28:29], v[20:21], s[40:41] op_sel:[0,1] op_sel_hi:[1,1]
	v_pk_mul_f32 v[30:31], v[22:23], s[40:41] op_sel:[0,1] op_sel_hi:[1,1]
	v_mfma_f32_32x32x16_f16 v[40:55], v[184:187], v[200:203], v[40:55]
	v_cmp_lt_i32_e64 s[60:61], 0, v92
	v_cmp_lt_i32_e64 s[62:63], 0, v93
	v_cmp_lt_i32_e64 s[64:65], 0, v94
	v_cmp_lt_i32_e64 s[66:67], 0, v95
	v_max_f32_e32 v24, v24, v28
	v_max_f32_e32 v25, v25, v29
	v_max_f32_e32 v26, v26, v30
	v_max_f32_e32 v27, v27, v31
	v_cndmask_b32_e64 v24, 0, v24, s[60:61]
	v_cndmask_b32_e64 v25, 0, v25, s[62:63]
	v_cndmask_b32_e64 v26, 0, v26, s[64:65]
	v_cndmask_b32_e64 v27, 0, v27, s[66:67]
	v_mfma_f32_32x32x16_f16 v[56:71], v[184:187], v[204:207], v[56:71]
	v_cvt_pkrtz_f16_f32 v34, v24, v25
	v_cvt_pkrtz_f16_f32 v35, v26, v27
	ds_write2_b64 v3, v[32:33], v[34:35] offset0:0 offset1:66
	v_pk_mul_f32 v[24:25], v[16:17], s[34:35] op_sel_hi:[1,0]
	v_pk_mul_f32 v[26:27], v[18:19], s[34:35] op_sel_hi:[1,0]
	v_pk_mul_f32 v[28:29], v[20:21], s[42:43] op_sel_hi:[1,0]
	v_pk_mul_f32 v[30:31], v[22:23], s[42:43] op_sel_hi:[1,0]
	v_mfma_f32_32x32x16_f16 v[72:87], v[184:187], v[12:15], v[72:87]
	v_cmp_lt_i32_e64 s[60:61], 0, v96
	v_cmp_lt_i32_e64 s[62:63], 0, v97
	v_cmp_lt_i32_e64 s[64:65], 0, v98
	v_cmp_lt_i32_e64 s[66:67], 0, v99
	v_max_f32_e32 v24, v24, v28
	v_max_f32_e32 v25, v25, v29
	v_max_f32_e32 v26, v26, v30
	v_max_f32_e32 v27, v27, v31
	v_cndmask_b32_e64 v24, 0, v24, s[60:61]
	v_cndmask_b32_e64 v25, 0, v25, s[62:63]
	v_cndmask_b32_e64 v26, 0, v26, s[64:65]
	v_cndmask_b32_e64 v27, 0, v27, s[66:67]
	v_mfma_f32_32x32x16_f16 v[40:55], v[188:191], v[208:211], v[40:55]
	v_cvt_pkrtz_f16_f32 v32, v24, v25
	v_cvt_pkrtz_f16_f32 v33, v26, v27
	v_pk_mul_f32 v[24:25], v[16:17], s[34:35] op_sel:[0,1] op_sel_hi:[1,1]
	v_pk_mul_f32 v[26:27], v[18:19], s[34:35] op_sel:[0,1] op_sel_hi:[1,1]
	v_pk_mul_f32 v[28:29], v[20:21], s[42:43] op_sel:[0,1] op_sel_hi:[1,1]
	v_pk_mul_f32 v[30:31], v[22:23], s[42:43] op_sel:[0,1] op_sel_hi:[1,1]
	v_mfma_f32_32x32x16_f16 v[56:71], v[188:191], v[212:215], v[56:71]
	v_cmp_lt_i32_e64 s[60:61], 0, v100
	v_cmp_lt_i32_e64 s[62:63], 0, v101
	v_cmp_lt_i32_e64 s[64:65], 0, v102
	v_cmp_lt_i32_e64 s[66:67], 0, v103
	v_max_f32_e32 v24, v24, v28
	v_max_f32_e32 v25, v25, v29
	v_max_f32_e32 v26, v26, v30
	v_max_f32_e32 v27, v27, v31
	v_cndmask_b32_e64 v24, 0, v24, s[60:61]
	v_cndmask_b32_e64 v25, 0, v25, s[62:63]
	v_cndmask_b32_e64 v26, 0, v26, s[64:65]
	v_cndmask_b32_e64 v27, 0, v27, s[66:67]
	v_mfma_f32_32x32x16_f16 v[72:87], v[188:191], v[12:15], v[72:87]
	v_cvt_pkrtz_f16_f32 v34, v24, v25
	v_cvt_pkrtz_f16_f32 v35, v26, v27
	ds_write2_b64 v3, v[32:33], v[34:35] offset0:132 offset1:198
	v_pk_mul_f32 v[24:25], v[16:17], s[36:37] op_sel_hi:[1,0]
	v_pk_mul_f32 v[26:27], v[18:19], s[36:37] op_sel_hi:[1,0]
	v_pk_mul_f32 v[28:29], v[20:21], s[44:45] op_sel_hi:[1,0]
	v_pk_mul_f32 v[30:31], v[22:23], s[44:45] op_sel_hi:[1,0]
	v_mfma_f32_32x32x16_f16 v[40:55], v[192:195], v[216:219], v[40:55]
	v_cmp_lt_i32_e64 s[60:61], 0, v104
	v_cmp_lt_i32_e64 s[62:63], 0, v105
	v_cmp_lt_i32_e64 s[64:65], 0, v106
	v_cmp_lt_i32_e64 s[66:67], 0, v107
	v_max_f32_e32 v24, v24, v28
	v_max_f32_e32 v25, v25, v29
	v_max_f32_e32 v26, v26, v30
	v_max_f32_e32 v27, v27, v31
	v_cndmask_b32_e64 v24, 0, v24, s[60:61]
	v_cndmask_b32_e64 v25, 0, v25, s[62:63]
	v_cndmask_b32_e64 v26, 0, v26, s[64:65]
	v_cndmask_b32_e64 v27, 0, v27, s[66:67]
	v_mfma_f32_32x32x16_f16 v[56:71], v[192:195], v[220:223], v[56:71]
	v_cvt_pkrtz_f16_f32 v32, v24, v25
	v_cvt_pkrtz_f16_f32 v33, v26, v27
	v_pk_mul_f32 v[24:25], v[16:17], s[36:37] op_sel:[0,1] op_sel_hi:[1,1]
	v_pk_mul_f32 v[26:27], v[18:19], s[36:37] op_sel:[0,1] op_sel_hi:[1,1]
	v_pk_mul_f32 v[28:29], v[20:21], s[44:45] op_sel:[0,1] op_sel_hi:[1,1]
	v_pk_mul_f32 v[30:31], v[22:23], s[44:45] op_sel:[0,1] op_sel_hi:[1,1]
	v_mfma_f32_32x32x16_f16 v[72:87], v[192:195], v[12:15], v[72:87]
	v_cmp_lt_i32_e64 s[60:61], 0, v108
	v_cmp_lt_i32_e64 s[62:63], 0, v109
	v_cmp_lt_i32_e64 s[64:65], 0, v110
	v_cmp_lt_i32_e64 s[66:67], 0, v111
	v_max_f32_e32 v24, v24, v28
	v_max_f32_e32 v25, v25, v29
	v_max_f32_e32 v26, v26, v30
	v_max_f32_e32 v27, v27, v31
	v_cndmask_b32_e64 v24, 0, v24, s[60:61]
	v_cndmask_b32_e64 v25, 0, v25, s[62:63]
	v_cndmask_b32_e64 v26, 0, v26, s[64:65]
	v_cndmask_b32_e64 v27, 0, v27, s[66:67]
	v_mfma_f32_32x32x16_f16 v[40:55], v[196:199], v[224:227], v[40:55]
	v_cvt_pkrtz_f16_f32 v34, v24, v25
	v_cvt_pkrtz_f16_f32 v35, v26, v27
	ds_write2_b64 v4, v[32:33], v[34:35] offset0:0 offset1:66
	v_pk_mul_f32 v[24:25], v[16:17], s[38:39] op_sel_hi:[1,0]
	v_pk_mul_f32 v[26:27], v[18:19], s[38:39] op_sel_hi:[1,0]
	v_pk_mul_f32 v[28:29], v[20:21], s[46:47] op_sel_hi:[1,0]
	v_pk_mul_f32 v[30:31], v[22:23], s[46:47] op_sel_hi:[1,0]
	v_mfma_f32_32x32x16_f16 v[56:71], v[196:199], v[228:231], v[56:71]
	v_cmp_lt_i32_e64 s[60:61], 0, v112
	v_cmp_lt_i32_e64 s[62:63], 0, v113
	v_cmp_lt_i32_e64 s[64:65], 0, v114
	v_cmp_lt_i32_e64 s[66:67], 0, v115
	v_max_f32_e32 v24, v24, v28
	v_max_f32_e32 v25, v25, v29
	v_max_f32_e32 v26, v26, v30
	v_max_f32_e32 v27, v27, v31
	v_cndmask_b32_e64 v24, 0, v24, s[60:61]
	v_cndmask_b32_e64 v25, 0, v25, s[62:63]
	v_cndmask_b32_e64 v26, 0, v26, s[64:65]
	v_cndmask_b32_e64 v27, 0, v27, s[66:67]
	v_cvt_pkrtz_f16_f32 v32, v24, v25
	v_cvt_pkrtz_f16_f32 v33, v26, v27
	v_pk_mul_f32 v[24:25], v[16:17], s[38:39] op_sel:[0,1] op_sel_hi:[1,1]
	v_pk_mul_f32 v[26:27], v[18:19], s[38:39] op_sel:[0,1] op_sel_hi:[1,1]
	v_pk_mul_f32 v[28:29], v[20:21], s[46:47] op_sel:[0,1] op_sel_hi:[1,1]
	v_pk_mul_f32 v[30:31], v[22:23], s[46:47] op_sel:[0,1] op_sel_hi:[1,1]
	v_mfma_f32_32x32x16_f16 v[72:87], v[196:199], v[12:15], v[72:87]
	v_cmp_lt_i32_e64 s[60:61], 0, v116
	v_cmp_lt_i32_e64 s[62:63], 0, v117
	v_cmp_lt_i32_e64 s[64:65], 0, v118
	v_cmp_lt_i32_e64 s[66:67], 0, v119
	v_max_f32_e32 v24, v24, v28
	v_max_f32_e32 v25, v25, v29
	v_max_f32_e32 v26, v26, v30
	v_max_f32_e32 v27, v27, v31
	v_cndmask_b32_e64 v24, 0, v24, s[60:61]
	v_cndmask_b32_e64 v25, 0, v25, s[62:63]
	v_cndmask_b32_e64 v26, 0, v26, s[64:65]
	v_cndmask_b32_e64 v27, 0, v27, s[66:67]
	v_cvt_pkrtz_f16_f32 v34, v24, v25
	v_cvt_pkrtz_f16_f32 v35, v26, v27
	ds_write2_b64 v4, v[32:33], v[34:35] offset0:132 offset1:198
	ds_write_b128 v9, v[152:155] offset:0
	ds_write_b128 v9, v[156:159] offset:1024
	ds_write_b128 v9, v[160:163] offset:2048
	ds_write_b128 v9, v[164:167] offset:3072
	s_add_u32 s3, s19, 7
	s_and_b32 s3, s3, 7
	s_lshl_b32 s3, s3, 10
	v_add_u32_e32 v11, s3, v10
	ds_read_b128 v[16:19], v11
	ds_read_b128 v[20:23], v11 offset:8192
	s_waitcnt lgkmcnt(0)
	s_barrier
	ds_read_b128 v[184:187], v7 offset:0
	ds_read_b128 v[200:203], v8 offset:0
	ds_read_b128 v[204:207], v8 offset:1024
	ds_read_b128 v[188:191], v7 offset:32
	ds_read_b128 v[208:211], v8 offset:2048
	ds_read_b128 v[212:215], v8 offset:3072
	ds_read_b128 v[192:195], v7 offset:64
	ds_read_b128 v[216:219], v8 offset:4096
	ds_read_b128 v[220:223], v8 offset:5120
	ds_read_b128 v[196:199], v7 offset:96
	ds_read_b128 v[224:227], v8 offset:6144
	ds_read_b128 v[228:231], v8 offset:7168
	s_waitcnt vmcnt(11)
	v_pk_mul_f32 v[24:25], v[16:17], s[32:33] op_sel_hi:[1,0]
	v_pk_mul_f32 v[26:27], v[18:19], s[32:33] op_sel_hi:[1,0]
	v_pk_mul_f32 v[28:29], v[20:21], s[40:41] op_sel_hi:[1,0]
	v_pk_mul_f32 v[30:31], v[22:23], s[40:41] op_sel_hi:[1,0]
	v_cmp_lt_i32_e64 s[60:61], 0, v120
	v_cmp_lt_i32_e64 s[62:63], 0, v121
	v_cmp_lt_i32_e64 s[64:65], 0, v122
	v_cmp_lt_i32_e64 s[66:67], 0, v123
	v_max_f32_e32 v24, v24, v28
	v_max_f32_e32 v25, v25, v29
	v_max_f32_e32 v26, v26, v30
	v_max_f32_e32 v27, v27, v31
	v_cndmask_b32_e64 v24, 0, v24, s[60:61]
	v_cndmask_b32_e64 v25, 0, v25, s[62:63]
	v_cndmask_b32_e64 v26, 0, v26, s[64:65]
	v_cndmask_b32_e64 v27, 0, v27, s[66:67]
	v_cvt_pkrtz_f16_f32 v32, v24, v25
	v_cvt_pkrtz_f16_f32 v33, v26, v27
	s_waitcnt vmcnt(10)
	s_waitcnt lgkmcnt(0)
	v_pk_mul_f32 v[24:25], v[16:17], s[32:33] op_sel:[0,1] op_sel_hi:[1,1]
	v_pk_mul_f32 v[26:27], v[18:19], s[32:33] op_sel:[0,1] op_sel_hi:[1,1]
	v_pk_mul_f32 v[28:29], v[20:21], s[40:41] op_sel:[0,1] op_sel_hi:[1,1]
	v_pk_mul_f32 v[30:31], v[22:23], s[40:41] op_sel:[0,1] op_sel_hi:[1,1]
	v_mfma_f32_32x32x16_f16 v[40:55], v[184:187], v[200:203], v[40:55]
	v_cmp_lt_i32_e64 s[60:61], 0, v124
	v_cmp_lt_i32_e64 s[62:63], 0, v125
	v_cmp_lt_i32_e64 s[64:65], 0, v126
	v_cmp_lt_i32_e64 s[66:67], 0, v127
	v_max_f32_e32 v24, v24, v28
	v_max_f32_e32 v25, v25, v29
	v_max_f32_e32 v26, v26, v30
	v_max_f32_e32 v27, v27, v31
	v_cndmask_b32_e64 v24, 0, v24, s[60:61]
	v_cndmask_b32_e64 v25, 0, v25, s[62:63]
	v_cndmask_b32_e64 v26, 0, v26, s[64:65]
	v_cndmask_b32_e64 v27, 0, v27, s[66:67]
	v_mfma_f32_32x32x16_f16 v[56:71], v[184:187], v[204:207], v[56:71]
	v_cvt_pkrtz_f16_f32 v34, v24, v25
	v_cvt_pkrtz_f16_f32 v35, v26, v27
	ds_write2_b64 v5, v[32:33], v[34:35] offset0:0 offset1:66
	s_waitcnt vmcnt(9)
	v_pk_mul_f32 v[24:25], v[16:17], s[34:35] op_sel_hi:[1,0]
	v_pk_mul_f32 v[26:27], v[18:19], s[34:35] op_sel_hi:[1,0]
	v_pk_mul_f32 v[28:29], v[20:21], s[42:43] op_sel_hi:[1,0]
	v_pk_mul_f32 v[30:31], v[22:23], s[42:43] op_sel_hi:[1,0]
	v_mfma_f32_32x32x16_f16 v[72:87], v[184:187], v[12:15], v[72:87]
	v_cmp_lt_i32_e64 s[60:61], 0, v128
	v_cmp_lt_i32_e64 s[62:63], 0, v129
	v_cmp_lt_i32_e64 s[64:65], 0, v130
	v_cmp_lt_i32_e64 s[66:67], 0, v131
	v_max_f32_e32 v24, v24, v28
	v_max_f32_e32 v25, v25, v29
	v_max_f32_e32 v26, v26, v30
	v_max_f32_e32 v27, v27, v31
	v_cndmask_b32_e64 v24, 0, v24, s[60:61]
	v_cndmask_b32_e64 v25, 0, v25, s[62:63]
	v_cndmask_b32_e64 v26, 0, v26, s[64:65]
	v_cndmask_b32_e64 v27, 0, v27, s[66:67]
	v_mfma_f32_32x32x16_f16 v[40:55], v[188:191], v[208:211], v[40:55]
	v_cvt_pkrtz_f16_f32 v32, v24, v25
	v_cvt_pkrtz_f16_f32 v33, v26, v27
	s_waitcnt vmcnt(8)
	v_pk_mul_f32 v[24:25], v[16:17], s[34:35] op_sel:[0,1] op_sel_hi:[1,1]
	v_pk_mul_f32 v[26:27], v[18:19], s[34:35] op_sel:[0,1] op_sel_hi:[1,1]
	v_pk_mul_f32 v[28:29], v[20:21], s[42:43] op_sel:[0,1] op_sel_hi:[1,1]
	v_pk_mul_f32 v[30:31], v[22:23], s[42:43] op_sel:[0,1] op_sel_hi:[1,1]
	v_mfma_f32_32x32x16_f16 v[56:71], v[188:191], v[212:215], v[56:71]
	v_cmp_lt_i32_e64 s[60:61], 0, v132
	v_cmp_lt_i32_e64 s[62:63], 0, v133
	v_cmp_lt_i32_e64 s[64:65], 0, v134
	v_cmp_lt_i32_e64 s[66:67], 0, v135
	v_max_f32_e32 v24, v24, v28
	v_max_f32_e32 v25, v25, v29
	v_max_f32_e32 v26, v26, v30
	v_max_f32_e32 v27, v27, v31
	v_cndmask_b32_e64 v24, 0, v24, s[60:61]
	v_cndmask_b32_e64 v25, 0, v25, s[62:63]
	v_cndmask_b32_e64 v26, 0, v26, s[64:65]
	v_cndmask_b32_e64 v27, 0, v27, s[66:67]
	v_mfma_f32_32x32x16_f16 v[72:87], v[188:191], v[12:15], v[72:87]
	v_cvt_pkrtz_f16_f32 v34, v24, v25
	v_cvt_pkrtz_f16_f32 v35, v26, v27
	ds_write2_b64 v5, v[32:33], v[34:35] offset0:132 offset1:198
	s_waitcnt vmcnt(7)
	v_pk_mul_f32 v[24:25], v[16:17], s[36:37] op_sel_hi:[1,0]
	v_pk_mul_f32 v[26:27], v[18:19], s[36:37] op_sel_hi:[1,0]
	v_pk_mul_f32 v[28:29], v[20:21], s[44:45] op_sel_hi:[1,0]
	v_pk_mul_f32 v[30:31], v[22:23], s[44:45] op_sel_hi:[1,0]
	v_mfma_f32_32x32x16_f16 v[40:55], v[192:195], v[216:219], v[40:55]
	v_cmp_lt_i32_e64 s[60:61], 0, v136
	v_cmp_lt_i32_e64 s[62:63], 0, v137
	v_cmp_lt_i32_e64 s[64:65], 0, v138
	v_cmp_lt_i32_e64 s[66:67], 0, v139
	v_max_f32_e32 v24, v24, v28
	v_max_f32_e32 v25, v25, v29
	v_max_f32_e32 v26, v26, v30
	v_max_f32_e32 v27, v27, v31
	v_cndmask_b32_e64 v24, 0, v24, s[60:61]
	v_cndmask_b32_e64 v25, 0, v25, s[62:63]
	v_cndmask_b32_e64 v26, 0, v26, s[64:65]
	v_cndmask_b32_e64 v27, 0, v27, s[66:67]
	v_mfma_f32_32x32x16_f16 v[56:71], v[192:195], v[220:223], v[56:71]
	v_cvt_pkrtz_f16_f32 v32, v24, v25
	v_cvt_pkrtz_f16_f32 v33, v26, v27
	s_waitcnt vmcnt(6)
	v_pk_mul_f32 v[24:25], v[16:17], s[36:37] op_sel:[0,1] op_sel_hi:[1,1]
	v_pk_mul_f32 v[26:27], v[18:19], s[36:37] op_sel:[0,1] op_sel_hi:[1,1]
	v_pk_mul_f32 v[28:29], v[20:21], s[44:45] op_sel:[0,1] op_sel_hi:[1,1]
	v_pk_mul_f32 v[30:31], v[22:23], s[44:45] op_sel:[0,1] op_sel_hi:[1,1]
	v_mfma_f32_32x32x16_f16 v[72:87], v[192:195], v[12:15], v[72:87]
	v_cmp_lt_i32_e64 s[60:61], 0, v140
	v_cmp_lt_i32_e64 s[62:63], 0, v141
	v_cmp_lt_i32_e64 s[64:65], 0, v142
	v_cmp_lt_i32_e64 s[66:67], 0, v143
	v_max_f32_e32 v24, v24, v28
	v_max_f32_e32 v25, v25, v29
	v_max_f32_e32 v26, v26, v30
	v_max_f32_e32 v27, v27, v31
	v_cndmask_b32_e64 v24, 0, v24, s[60:61]
	v_cndmask_b32_e64 v25, 0, v25, s[62:63]
	v_cndmask_b32_e64 v26, 0, v26, s[64:65]
	v_cndmask_b32_e64 v27, 0, v27, s[66:67]
	v_mfma_f32_32x32x16_f16 v[40:55], v[196:199], v[224:227], v[40:55]
	v_cvt_pkrtz_f16_f32 v34, v24, v25
	v_cvt_pkrtz_f16_f32 v35, v26, v27
	ds_write2_b64 v6, v[32:33], v[34:35] offset0:0 offset1:66
	s_waitcnt vmcnt(5)
	v_pk_mul_f32 v[24:25], v[16:17], s[38:39] op_sel_hi:[1,0]
	v_pk_mul_f32 v[26:27], v[18:19], s[38:39] op_sel_hi:[1,0]
	v_pk_mul_f32 v[28:29], v[20:21], s[46:47] op_sel_hi:[1,0]
	v_pk_mul_f32 v[30:31], v[22:23], s[46:47] op_sel_hi:[1,0]
	v_mfma_f32_32x32x16_f16 v[56:71], v[196:199], v[228:231], v[56:71]
	v_cmp_lt_i32_e64 s[60:61], 0, v144
	v_cmp_lt_i32_e64 s[62:63], 0, v145
	v_cmp_lt_i32_e64 s[64:65], 0, v146
	v_cmp_lt_i32_e64 s[66:67], 0, v147
	v_max_f32_e32 v24, v24, v28
	v_max_f32_e32 v25, v25, v29
	v_max_f32_e32 v26, v26, v30
	v_max_f32_e32 v27, v27, v31
	v_cndmask_b32_e64 v24, 0, v24, s[60:61]
	v_cndmask_b32_e64 v25, 0, v25, s[62:63]
	v_cndmask_b32_e64 v26, 0, v26, s[64:65]
	v_cndmask_b32_e64 v27, 0, v27, s[66:67]
	v_cvt_pkrtz_f16_f32 v32, v24, v25
	v_cvt_pkrtz_f16_f32 v33, v26, v27
	s_waitcnt vmcnt(4)
	v_pk_mul_f32 v[24:25], v[16:17], s[38:39] op_sel:[0,1] op_sel_hi:[1,1]
	v_pk_mul_f32 v[26:27], v[18:19], s[38:39] op_sel:[0,1] op_sel_hi:[1,1]
	v_pk_mul_f32 v[28:29], v[20:21], s[46:47] op_sel:[0,1] op_sel_hi:[1,1]
	v_pk_mul_f32 v[30:31], v[22:23], s[46:47] op_sel:[0,1] op_sel_hi:[1,1]
	v_mfma_f32_32x32x16_f16 v[72:87], v[196:199], v[12:15], v[72:87]
	v_cmp_lt_i32_e64 s[60:61], 0, v148
	v_cmp_lt_i32_e64 s[62:63], 0, v149
	v_cmp_lt_i32_e64 s[64:65], 0, v150
	v_cmp_lt_i32_e64 s[66:67], 0, v151
	v_max_f32_e32 v24, v24, v28
	v_max_f32_e32 v25, v25, v29
	v_max_f32_e32 v26, v26, v30
	v_max_f32_e32 v27, v27, v31
	v_cndmask_b32_e64 v24, 0, v24, s[60:61]
	v_cndmask_b32_e64 v25, 0, v25, s[62:63]
	v_cndmask_b32_e64 v26, 0, v26, s[64:65]
	v_cndmask_b32_e64 v27, 0, v27, s[66:67]
	v_cvt_pkrtz_f16_f32 v34, v24, v25
	v_cvt_pkrtz_f16_f32 v35, v26, v27
	ds_write2_b64 v6, v[32:33], v[34:35] offset0:132 offset1:198
	s_waitcnt vmcnt(0)
	ds_write_b128 v9, v[168:171] offset:32768
	ds_write_b128 v9, v[172:175] offset:33792
	ds_write_b128 v9, v[176:179] offset:34816
	ds_write_b128 v9, v[180:183] offset:35840
	s_waitcnt lgkmcnt(0)
	s_barrier
	ds_read_b128 v[184:187], v7 offset:33792
	ds_read_b128 v[200:203], v8 offset:32768
	ds_read_b128 v[204:207], v8 offset:33792
	ds_read_b128 v[188:191], v7 offset:33824
	ds_read_b128 v[208:211], v8 offset:34816
	ds_read_b128 v[212:215], v8 offset:35840
	ds_read_b128 v[192:195], v7 offset:33856
	ds_read_b128 v[216:219], v8 offset:36864
	ds_read_b128 v[220:223], v8 offset:37888
	ds_read_b128 v[196:199], v7 offset:33888
	ds_read_b128 v[224:227], v8 offset:38912
	ds_read_b128 v[228:231], v8 offset:39936
	s_waitcnt lgkmcnt(0)
	v_mfma_f32_32x32x16_f16 v[40:55], v[184:187], v[200:203], v[40:55]
	v_mfma_f32_32x32x16_f16 v[56:71], v[184:187], v[204:207], v[56:71]
	v_mfma_f32_32x32x16_f16 v[72:87], v[184:187], v[12:15], v[72:87]
	v_mfma_f32_32x32x16_f16 v[40:55], v[188:191], v[208:211], v[40:55]
	v_mfma_f32_32x32x16_f16 v[56:71], v[188:191], v[212:215], v[56:71]
	v_mfma_f32_32x32x16_f16 v[72:87], v[188:191], v[12:15], v[72:87]
	v_mfma_f32_32x32x16_f16 v[40:55], v[192:195], v[216:219], v[40:55]
	v_mfma_f32_32x32x16_f16 v[56:71], v[192:195], v[220:223], v[56:71]
	v_mfma_f32_32x32x16_f16 v[72:87], v[192:195], v[12:15], v[72:87]
	v_mfma_f32_32x32x16_f16 v[40:55], v[196:199], v[224:227], v[40:55]
	v_mfma_f32_32x32x16_f16 v[56:71], v[196:199], v[228:231], v[56:71]
	v_mfma_f32_32x32x16_f16 v[72:87], v[196:199], v[12:15], v[72:87]
	s_nop 11
	s_cmp_eq_u32 s21, 0
	s_cbranch_scc0 .Lgm_red_not0
	s_lshl_b32 s3, s20, 2
	s_add_u32 s3, s3, 1
	s_mul_i32 s57, s3, 0x2400
	s_cmp_ge_u32 s3, 3
	s_cselect_b32 s58, 0x9c00, 0
	s_add_u32 s57, s57, s58
	v_add_u32_e32 v36, s57, v1
	s_lshl_b32 s3, s20, 2
	s_add_u32 s3, s3, 2
	s_mul_i32 s57, s3, 0x2400
	s_cmp_ge_u32 s3, 3
	s_cselect_b32 s58, 0x9c00, 0
	s_add_u32 s57, s57, s58
	v_add_u32_e32 v37, s57, v1
	s_lshl_b32 s3, s20, 2
	s_add_u32 s3, s3, 3
	s_mul_i32 s57, s3, 0x2400
	s_cmp_ge_u32 s3, 3
	s_cselect_b32 s58, 0x9c00, 0
	s_add_u32 s57, s57, s58
	v_add_u32_e32 v38, s57, v1
	ds_write_b128 v36, v[44:47] offset:0
	ds_write_b128 v36, v[60:63] offset:1024
	ds_write_b128 v36, v[76:79] offset:2048
	ds_write_b128 v37, v[48:51] offset:0
	ds_write_b128 v37, v[64:67] offset:1024
	ds_write_b128 v37, v[80:83] offset:2048
	ds_write_b128 v38, v[52:55] offset:0
	ds_write_b128 v38, v[68:71] offset:1024
	ds_write_b128 v38, v[84:87] offset:2048
	s_waitcnt lgkmcnt(0)
	s_barrier
	s_mov_b32 s3, s16
	s_mul_i32 s57, s3, 0x2400
	s_cmp_ge_u32 s3, 3
	s_cselect_b32 s58, 0x9c00, 0
	s_add_u32 s57, s57, s58
	v_add_u32_e32 v36, s57, v1
	ds_read_b128 v[88:91], v36 offset:0
	ds_read_b128 v[92:95], v36 offset:1024
	ds_read_b128 v[96:99], v36 offset:2048
	ds_read_b128 v[100:103], v36 offset:3072
	ds_read_b128 v[104:107], v36 offset:4096
	ds_read_b128 v[108:111], v36 offset:5120
	ds_read_b128 v[112:115], v36 offset:6144
	ds_read_b128 v[116:119], v36 offset:7168
	ds_read_b128 v[120:123], v36 offset:8192
	s_waitcnt lgkmcnt(0)
	v_add_f32_e32 v40, v40, v88
	v_add_f32_e32 v41, v41, v89
	v_add_f32_e32 v42, v42, v90
	v_add_f32_e32 v43, v43, v91
	v_add_f32_e32 v40, v40, v100
	v_add_f32_e32 v41, v41, v101
	v_add_f32_e32 v42, v42, v102
	v_add_f32_e32 v43, v43, v103
	v_add_f32_e32 v40, v40, v112
	v_add_f32_e32 v41, v41, v113
	v_add_f32_e32 v42, v42, v114
	v_add_f32_e32 v43, v43, v115
	v_add_f32_e32 v44, v56, v92
	v_add_f32_e32 v45, v57, v93
	v_add_f32_e32 v46, v58, v94
	v_add_f32_e32 v47, v59, v95
	v_add_f32_e32 v44, v44, v104
	v_add_f32_e32 v45, v45, v105
	v_add_f32_e32 v46, v46, v106
	v_add_f32_e32 v47, v47, v107
	v_add_f32_e32 v44, v44, v116
	v_add_f32_e32 v45, v45, v117
	v_add_f32_e32 v46, v46, v118
	v_add_f32_e32 v47, v47, v119
	v_add_f32_e32 v48, v72, v96
	v_add_f32_e32 v49, v73, v97
	v_add_f32_e32 v50, v74, v98
	v_add_f32_e32 v51, v75, v99
	v_add_f32_e32 v48, v48, v108
	v_add_f32_e32 v49, v49, v109
	v_add_f32_e32 v50, v50, v110
	v_add_f32_e32 v51, v51, v111
	v_add_f32_e32 v48, v48, v120
	v_add_f32_e32 v49, v49, v121
	v_add_f32_e32 v50, v50, v122
	v_add_f32_e32 v51, v51, v123
	s_branch .Lgm_red_done
